# stack12 + lagging wave-half re-alignment barrier moved behind the next unit's scalar header decode (8 GEMM phases), flag in s101
# baseline (speedup 1.0000x reference)
.LBB0_150:
	s_mov_b32 s101, 0
	v_readlane_b32 s2, v254, 16
	v_readlane_b32 s3, v254, 17
	s_cmp_lt_i32 s2, 2
	s_cselect_b64 s[2:3], -1, 0
	s_add_u32 s4, s86, 0x1d800000
	s_addc_u32 s5, s87, 0
	v_writelane_b32 v254, s4, 18
	s_and_b64 s[0:1], s[2:3], s[0:1]
	s_mov_b32 s2, s66
	v_writelane_b32 v254, s5, 19
	v_writelane_b32 v254, s2, 20
	s_andn2_b64 vcc, exec, s[0:1]
	s_nop 0
	v_writelane_b32 v254, s3, 21
	s_cbranch_vccnz .LBB0_355
	v_readlane_b32 s2, v254, 14
	s_cmpk_lt_i32 s2, 0xa00
	s_cselect_b64 s[4:5], -1, 0
	s_cmpk_gt_i32 s2, 0x9ff
	v_readfirstlane_b32 s8, v0
	s_cbranch_scc1 .LBB0_153
	v_readlane_b32 s6, v254, 14
	s_ashr_i32 s2, s6, 31
	s_lshr_b32 s2, s2, 29
	s_add_i32 s2, s6, s2
	s_ashr_i32 s3, s2, 3
	s_and_b32 s2, s2, -8
	s_sub_i32 s2, s6, s2
	s_cmp_lt_i32 s2, 0
	s_movk_i32 s6, 0x141
	s_cselect_b32 s6, s6, 0x140
	s_mul_i32 s2, s2, s6
	s_add_i32 s2, s2, s3
	s_mul_hi_i32 s3, s2, 0x66666667
	s_lshr_b32 s6, s3, 31
	s_ashr_i32 s3, s3, 6
	s_add_i32 s3, s3, s6
	s_lshl_b32 s6, s3, 3
	s_mulk_i32 s3, 0xa0
	s_sub_i32 s2, s2, s3
	s_sext_i32_i16 s3, s2
	s_bfe_u32 s3, s3, 0x3001c
	s_add_i32 s3, s2, s3
	s_sext_i32_i16 s7, s3
	s_and_b32 s3, s3, 0xfff8
	s_sub_i32 s2, s2, s3
	s_sext_i32_i16 s2, s2
	s_add_i32 s2, s6, s2
	s_ashr_i32 s14, s7, 3

.LBB0_161:
	s_ashr_i32 s29, s28, 31
	s_lshl_b64 s[30:31], s[28:29], 20
	v_readlane_b32 s34, v254, 18
	v_readlane_b32 s35, v254, 19
	s_add_u32 s30, s34, s30
	s_addc_u32 s31, s35, s31
	s_and_b64 s[34:35], s[12:13], exec
	s_cselect_b32 s15, s31, s17
	s_cselect_b32 s29, s30, s16
	s_ashr_i32 s27, s26, 31
	s_lshl_b64 s[34:35], s[26:27], 20
	s_add_u32 s34, s33, s34
	s_addc_u32 s35, s42, s35
	s_and_b64 s[38:39], s[12:13], exec
	s_cselect_b32 s27, s35, s37
	s_cselect_b32 s40, s34, s36
	s_add_u32 s16, s16, 0x80080
	s_addc_u32 s17, s17, 0
	s_add_u32 s41, s36, 0x100
	s_addc_u32 s64, s37, 0
	s_mov_b32 s65, -2
	s_cmp_lg_u32 s101, 0
	s_cbranch_scc0 .Lbs_162
	s_barrier
	s_mov_b32 s101, 0
.Lbs_162:
	ds_read_b128 v[90:93], v197
	ds_read_b128 v[94:97], v197 offset:1024
	ds_read_b128 v[98:101], v197 offset:2048
	ds_read_b128 v[102:105], v197 offset:3072
	ds_read_b128 v[146:149], v198
	ds_read_b128 v[150:153], v198 offset:1024
	ds_read_b128 v[180:183], v198 offset:2048
	ds_read_b128 v[184:187], v198 offset:3072
	s_add_u32 s36, s16, 0xfff80080
	s_addc_u32 s37, s17, -1
	s_cmp_eq_u32 s65, 28
	s_cselect_b32 s39, s15, s37
	s_cselect_b32 s38, s29, s36
	s_cselect_b32 s37, s27, s64
	s_cselect_b32 s36, s40, s41
	v_lshl_add_u64 v[212:213], s[16:17], 0, v[172:173]
	s_add_i32 m0, s44, 0xc000
	ds_read_b128 v[188:191], v199
	ds_read_b128 v[192:195], v199 offset:1024
	ds_read_b128 v[200:203], v199 offset:2048
	ds_read_b128 v[204:207], v199 offset:3072
	ds_read_b128 v[208:211], v199 offset:4096
	ds_read_b128 v[216:219], v199 offset:5120
	ds_read_b128 v[220:223], v199 offset:6144
	ds_read_b128 v[224:227], v199 offset:7168
	global_load_lds_dwordx4 v[212:213], off
	v_lshl_add_u64 v[212:213], s[16:17], 0, v[174:175]
	s_add_i32 m0, s44, 0xe000
	s_nop 0
	global_load_lds_dwordx4 v[212:213], off
	s_waitcnt vmcnt(8)
	s_waitcnt lgkmcnt(0)
	s_setprio 1
	s_barrier
	v_mfma_f32_16x16x32_bf16 v[70:73], v[90:93], v[188:191], 0
	v_mfma_f32_16x16x32_bf16 v[66:69], v[98:101], v[188:191], 0
	v_mfma_f32_16x16x32_bf16 v[54:57], v[90:93], v[200:203], 0
	v_mfma_f32_16x16x32_bf16 v[50:53], v[98:101], v[200:203], 0
	v_mfma_f32_16x16x32_bf16 v[46:49], v[90:93], v[208:211], 0
	v_mfma_f32_16x16x32_bf16 v[42:45], v[98:101], v[208:211], 0
	v_mfma_f32_16x16x32_bf16 v[38:41], v[90:93], v[220:223], 0
	v_mfma_f32_16x16x32_bf16 v[34:37], v[98:101], v[220:223], 0
	v_mfma_f32_16x16x32_bf16 v[70:73], v[94:97], v[192:195], v[70:73]
	v_mfma_f32_16x16x32_bf16 v[66:69], v[102:105], v[192:195], v[66:69]
	v_mfma_f32_16x16x32_bf16 v[54:57], v[94:97], v[204:207], v[54:57]
	v_mfma_f32_16x16x32_bf16 v[50:53], v[102:105], v[204:207], v[50:53]
	v_mfma_f32_16x16x32_bf16 v[46:49], v[94:97], v[216:219], v[46:49]
	v_mfma_f32_16x16x32_bf16 v[42:45], v[102:105], v[216:219], v[42:45]
	v_mfma_f32_16x16x32_bf16 v[38:41], v[94:97], v[224:227], v[38:41]
	v_mfma_f32_16x16x32_bf16 v[34:37], v[102:105], v[224:227], v[34:37]
	s_setprio 0
	s_setprio 1
	v_mfma_f32_16x16x32_bf16 v[142:145], v[146:149], v[188:191], 0
	v_mfma_f32_16x16x32_bf16 v[138:141], v[180:183], v[188:191], 0
	v_mfma_f32_16x16x32_bf16 v[134:137], v[146:149], v[200:203], 0
	v_mfma_f32_16x16x32_bf16 v[130:133], v[180:183], v[200:203], 0
	v_mfma_f32_16x16x32_bf16 v[126:129], v[146:149], v[208:211], 0
	v_mfma_f32_16x16x32_bf16 v[122:125], v[180:183], v[208:211], 0
	v_mfma_f32_16x16x32_bf16 v[118:121], v[146:149], v[220:223], 0
	v_mfma_f32_16x16x32_bf16 v[114:117], v[180:183], v[220:223], 0
	v_mfma_f32_16x16x32_bf16 v[142:145], v[150:153], v[192:195], v[142:145]
	v_mfma_f32_16x16x32_bf16 v[138:141], v[184:187], v[192:195], v[138:141]
	v_mfma_f32_16x16x32_bf16 v[134:137], v[150:153], v[204:207], v[134:137]
	v_mfma_f32_16x16x32_bf16 v[130:133], v[184:187], v[204:207], v[130:133]
	v_mfma_f32_16x16x32_bf16 v[126:129], v[150:153], v[216:219], v[126:129]
	v_mfma_f32_16x16x32_bf16 v[122:125], v[184:187], v[216:219], v[122:125]
	v_mfma_f32_16x16x32_bf16 v[118:121], v[150:153], v[224:227], v[118:121]
	v_mfma_f32_16x16x32_bf16 v[114:117], v[184:187], v[224:227], v[114:117]
	s_barrier
	s_setprio 0
	s_add_i32 s66, s57, s43
	v_lshl_add_u64 v[212:213], s[36:37], 0, v[156:157]
	s_mov_b32 m0, s66
	ds_read_b128 v[188:191], v199 offset:16384
	ds_read_b128 v[192:195], v199 offset:17408
	ds_read_b128 v[200:203], v199 offset:18432
	ds_read_b128 v[204:207], v199 offset:19456
	ds_read_b128 v[208:211], v199 offset:20480
	ds_read_b128 v[216:219], v199 offset:21504
	ds_read_b128 v[220:223], v199 offset:22528
	ds_read_b128 v[224:227], v199 offset:23552
	global_load_lds_dwordx4 v[212:213], off
	s_add_i32 m0, s66, 0x2000
	s_add_u32 s66, s36, 0x80000
	v_lshl_add_u64 v[214:215], s[36:37], 0, v[160:161]
	s_addc_u32 s67, s37, 0
	s_add_i32 s68, s58, s43
	global_load_lds_dwordx4 v[214:215], off
	v_lshl_add_u64 v[228:229], s[66:67], 0, v[156:157]
	s_mov_b32 m0, s68
	v_lshl_add_u64 v[230:231], s[38:39], 0, v[158:159]
	global_load_lds_dwordx4 v[228:229], off
	v_lshl_add_u64 v[228:229], s[66:67], 0, v[160:161]
	s_add_i32 m0, s68, 0x2000
	s_nop 0
	global_load_lds_dwordx4 v[228:229], off
	v_lshl_add_u64 v[228:229], s[38:39], 0, v[154:155]
	s_mov_b32 m0, s44
	s_nop 0
	global_load_lds_dwordx4 v[228:229], off
	s_mov_b32 m0, s45
	s_nop 0
	global_load_lds_dwordx4 v[230:231], off
	s_waitcnt vmcnt(8)
	s_waitcnt lgkmcnt(0)
	s_setprio 1
	s_barrier
	v_mfma_f32_16x16x32_bf16 v[30:33], v[90:93], v[188:191], 0
	v_mfma_f32_16x16x32_bf16 v[26:29], v[98:101], v[188:191], 0
	v_mfma_f32_16x16x32_bf16 v[22:25], v[90:93], v[200:203], 0
	v_mfma_f32_16x16x32_bf16 v[18:21], v[98:101], v[200:203], 0
	v_mfma_f32_16x16x32_bf16 v[14:17], v[90:93], v[208:211], 0
	v_mfma_f32_16x16x32_bf16 v[10:13], v[98:101], v[208:211], 0
	v_mfma_f32_16x16x32_bf16 v[6:9], v[90:93], v[220:223], 0
	v_mfma_f32_16x16x32_bf16 v[2:5], v[98:101], v[220:223], 0
	v_mfma_f32_16x16x32_bf16 v[30:33], v[94:97], v[192:195], v[30:33]
	v_mfma_f32_16x16x32_bf16 v[26:29], v[102:105], v[192:195], v[26:29]
	v_mfma_f32_16x16x32_bf16 v[22:25], v[94:97], v[204:207], v[22:25]
	v_mfma_f32_16x16x32_bf16 v[18:21], v[102:105], v[204:207], v[18:21]
	v_mfma_f32_16x16x32_bf16 v[14:17], v[94:97], v[216:219], v[14:17]
	v_mfma_f32_16x16x32_bf16 v[10:13], v[102:105], v[216:219], v[10:13]
	v_mfma_f32_16x16x32_bf16 v[6:9], v[94:97], v[224:227], v[6:9]
	v_mfma_f32_16x16x32_bf16 v[2:5], v[102:105], v[224:227], v[2:5]
	s_setprio 0
	s_setprio 1
	v_mfma_f32_16x16x32_bf16 v[86:89], v[146:149], v[200:203], 0
	v_mfma_f32_16x16x32_bf16 v[82:85], v[180:183], v[200:203], 0
	v_mfma_f32_16x16x32_bf16 v[78:81], v[146:149], v[208:211], 0
	v_mfma_f32_16x16x32_bf16 v[74:77], v[180:183], v[208:211], 0
	v_mfma_f32_16x16x32_bf16 v[62:65], v[146:149], v[220:223], 0
	v_mfma_f32_16x16x32_bf16 v[58:61], v[180:183], v[220:223], 0
	v_mfma_f32_16x16x32_bf16 v[90:93], v[146:149], v[188:191], 0
	v_mfma_f32_16x16x32_bf16 v[94:97], v[180:183], v[188:191], 0
	v_mfma_f32_16x16x32_bf16 v[86:89], v[150:153], v[204:207], v[86:89]
	v_mfma_f32_16x16x32_bf16 v[82:85], v[184:187], v[204:207], v[82:85]
	v_mfma_f32_16x16x32_bf16 v[78:81], v[150:153], v[216:219], v[78:81]
	v_mfma_f32_16x16x32_bf16 v[74:77], v[184:187], v[216:219], v[74:77]
	v_mfma_f32_16x16x32_bf16 v[62:65], v[150:153], v[224:227], v[62:65]
	v_mfma_f32_16x16x32_bf16 v[58:61], v[184:187], v[224:227], v[58:61]
	v_mfma_f32_16x16x32_bf16 v[90:93], v[150:153], v[192:195], v[90:93]
	v_mfma_f32_16x16x32_bf16 v[94:97], v[184:187], v[192:195], v[94:97]
	s_barrier
	s_setprio 0
	s_add_i32 s66, 0, 0x18000
	s_add_i32 s67, 0, 0x1c000
	v_add_u32_e32 v110, s66, v165
	v_add_u32_e32 v162, s67, v165
	ds_read_b128 v[98:101], v110
	ds_read_b128 v[102:105], v110 offset:1024
	ds_read_b128 v[106:109], v110 offset:2048
	ds_read_b128 v[110:113], v110 offset:3072
	ds_read_b128 v[146:149], v162
	ds_read_b128 v[150:153], v162 offset:1024
	ds_read_b128 v[180:183], v162 offset:2048
	ds_read_b128 v[184:187], v162 offset:3072
	s_add_u32 s38, s38, 0x80000
	s_addc_u32 s39, s39, 0
	s_mov_b32 m0, s47
	v_lshl_add_u64 v[232:233], s[38:39], 0, v[154:155]
	ds_read_b128 v[188:191], v199 offset:32768
	ds_read_b128 v[192:195], v199 offset:33792
	ds_read_b128 v[200:203], v199 offset:34816
	ds_read_b128 v[204:207], v199 offset:35840
	ds_read_b128 v[208:211], v199 offset:36864
	ds_read_b128 v[216:219], v199 offset:37888
	ds_read_b128 v[220:223], v199 offset:38912
	ds_read_b128 v[224:227], v199 offset:39936
	global_load_lds_dwordx4 v[232:233], off
	v_lshl_add_u64 v[232:233], s[38:39], 0, v[158:159]
	s_mov_b32 m0, s48
	s_nop 0
	global_load_lds_dwordx4 v[232:233], off
	s_waitcnt vmcnt(8)
	s_waitcnt lgkmcnt(0)
	s_setprio 1
	s_barrier
	v_mfma_f32_16x16x32_bf16 v[70:73], v[98:101], v[188:191], v[70:73]
	v_mfma_f32_16x16x32_bf16 v[66:69], v[106:109], v[188:191], v[66:69]
	v_mfma_f32_16x16x32_bf16 v[54:57], v[98:101], v[200:203], v[54:57]
	v_mfma_f32_16x16x32_bf16 v[50:53], v[106:109], v[200:203], v[50:53]
	v_mfma_f32_16x16x32_bf16 v[46:49], v[98:101], v[208:211], v[46:49]
	v_mfma_f32_16x16x32_bf16 v[42:45], v[106:109], v[208:211], v[42:45]
	v_mfma_f32_16x16x32_bf16 v[38:41], v[98:101], v[220:223], v[38:41]
	v_mfma_f32_16x16x32_bf16 v[34:37], v[106:109], v[220:223], v[34:37]
	v_mfma_f32_16x16x32_bf16 v[70:73], v[102:105], v[192:195], v[70:73]
	v_mfma_f32_16x16x32_bf16 v[66:69], v[110:113], v[192:195], v[66:69]
	v_mfma_f32_16x16x32_bf16 v[54:57], v[102:105], v[204:207], v[54:57]
	v_mfma_f32_16x16x32_bf16 v[50:53], v[110:113], v[204:207], v[50:53]
	v_mfma_f32_16x16x32_bf16 v[46:49], v[102:105], v[216:219], v[46:49]
	v_mfma_f32_16x16x32_bf16 v[42:45], v[110:113], v[216:219], v[42:45]
	v_mfma_f32_16x16x32_bf16 v[38:41], v[102:105], v[224:227], v[38:41]
	v_mfma_f32_16x16x32_bf16 v[34:37], v[110:113], v[224:227], v[34:37]
	s_setprio 0
	s_setprio 1
	v_mfma_f32_16x16x32_bf16 v[142:145], v[146:149], v[188:191], v[142:145]
	v_mfma_f32_16x16x32_bf16 v[138:141], v[180:183], v[188:191], v[138:141]
	v_mfma_f32_16x16x32_bf16 v[134:137], v[146:149], v[200:203], v[134:137]
	v_mfma_f32_16x16x32_bf16 v[130:133], v[180:183], v[200:203], v[130:133]
	v_mfma_f32_16x16x32_bf16 v[126:129], v[146:149], v[208:211], v[126:129]
	v_mfma_f32_16x16x32_bf16 v[122:125], v[180:183], v[208:211], v[122:125]
	v_mfma_f32_16x16x32_bf16 v[118:121], v[146:149], v[220:223], v[118:121]
	v_mfma_f32_16x16x32_bf16 v[114:117], v[180:183], v[220:223], v[114:117]
	v_mfma_f32_16x16x32_bf16 v[142:145], v[150:153], v[192:195], v[142:145]
	v_mfma_f32_16x16x32_bf16 v[138:141], v[184:187], v[192:195], v[138:141]
	v_mfma_f32_16x16x32_bf16 v[134:137], v[150:153], v[204:207], v[134:137]
	v_mfma_f32_16x16x32_bf16 v[130:133], v[184:187], v[204:207], v[130:133]
	v_mfma_f32_16x16x32_bf16 v[126:129], v[150:153], v[216:219], v[126:129]
	v_mfma_f32_16x16x32_bf16 v[122:125], v[184:187], v[216:219], v[122:125]
	v_mfma_f32_16x16x32_bf16 v[118:121], v[150:153], v[224:227], v[118:121]
	v_mfma_f32_16x16x32_bf16 v[114:117], v[184:187], v[224:227], v[114:117]
	s_barrier
	s_setprio 0
	s_add_i32 s38, s66, s43
	v_lshl_add_u64 v[212:213], v[212:213], 0, s[18:19]
	s_mov_b32 m0, s38
	ds_read_b128 v[188:191], v199 offset:49152
	ds_read_b128 v[192:195], v199 offset:50176
	ds_read_b128 v[200:203], v199 offset:51200
	ds_read_b128 v[204:207], v199 offset:52224
	ds_read_b128 v[208:211], v199 offset:53248
	ds_read_b128 v[216:219], v199 offset:54272
	ds_read_b128 v[220:223], v199 offset:55296
	ds_read_b128 v[224:227], v199 offset:56320
	global_load_lds_dwordx4 v[212:213], off
	s_add_i32 m0, s38, 0x2000
	s_add_u32 s36, s36, 0x80080
	v_lshl_add_u64 v[212:213], v[214:215], 0, s[18:19]
	s_addc_u32 s37, s37, 0
	s_add_i32 s38, s67, s43
	global_load_lds_dwordx4 v[212:213], off
	v_lshl_add_u64 v[212:213], s[36:37], 0, v[156:157]
	s_mov_b32 m0, s38
	s_nop 0
	global_load_lds_dwordx4 v[212:213], off
	v_lshl_add_u64 v[212:213], s[36:37], 0, v[160:161]
	s_add_i32 m0, s38, 0x2000
	s_nop 0
	global_load_lds_dwordx4 v[212:213], off
	v_lshl_add_u64 v[212:213], v[228:229], 0, s[18:19]
	s_mov_b32 m0, s52
	s_nop 0
	global_load_lds_dwordx4 v[212:213], off
	v_lshl_add_u64 v[212:213], v[230:231], 0, s[18:19]
	s_mov_b32 m0, s53
	s_nop 0
	global_load_lds_dwordx4 v[212:213], off
	s_waitcnt vmcnt(8)
	s_waitcnt lgkmcnt(0)
	s_setprio 1
	s_barrier
	v_mfma_f32_16x16x32_bf16 v[30:33], v[98:101], v[188:191], v[30:33]
	v_mfma_f32_16x16x32_bf16 v[26:29], v[106:109], v[188:191], v[26:29]
	v_mfma_f32_16x16x32_bf16 v[22:25], v[98:101], v[200:203], v[22:25]
	v_mfma_f32_16x16x32_bf16 v[18:21], v[106:109], v[200:203], v[18:21]
	v_mfma_f32_16x16x32_bf16 v[14:17], v[98:101], v[208:211], v[14:17]
	v_mfma_f32_16x16x32_bf16 v[10:13], v[106:109], v[208:211], v[10:13]
	v_mfma_f32_16x16x32_bf16 v[6:9], v[98:101], v[220:223], v[6:9]
	v_mfma_f32_16x16x32_bf16 v[2:5], v[106:109], v[220:223], v[2:5]
	v_mfma_f32_16x16x32_bf16 v[30:33], v[102:105], v[192:195], v[30:33]
	v_mfma_f32_16x16x32_bf16 v[26:29], v[110:113], v[192:195], v[26:29]
	v_mfma_f32_16x16x32_bf16 v[22:25], v[102:105], v[204:207], v[22:25]
	v_mfma_f32_16x16x32_bf16 v[18:21], v[110:113], v[204:207], v[18:21]
	v_mfma_f32_16x16x32_bf16 v[14:17], v[102:105], v[216:219], v[14:17]
	v_mfma_f32_16x16x32_bf16 v[10:13], v[110:113], v[216:219], v[10:13]
	v_mfma_f32_16x16x32_bf16 v[6:9], v[102:105], v[224:227], v[6:9]
	v_mfma_f32_16x16x32_bf16 v[2:5], v[110:113], v[224:227], v[2:5]
	s_setprio 0
	s_setprio 1
	v_mfma_f32_16x16x32_bf16 v[90:93], v[146:149], v[188:191], v[90:93]
	v_mfma_f32_16x16x32_bf16 v[110:113], v[150:153], v[192:195], v[90:93]
	v_mfma_f32_16x16x32_bf16 v[90:93], v[180:183], v[188:191], v[94:97]
	v_mfma_f32_16x16x32_bf16 v[86:89], v[146:149], v[200:203], v[86:89]
	v_mfma_f32_16x16x32_bf16 v[82:85], v[180:183], v[200:203], v[82:85]
	v_mfma_f32_16x16x32_bf16 v[78:81], v[146:149], v[208:211], v[78:81]
	v_mfma_f32_16x16x32_bf16 v[74:77], v[180:183], v[208:211], v[74:77]
	v_mfma_f32_16x16x32_bf16 v[62:65], v[146:149], v[220:223], v[62:65]
	v_mfma_f32_16x16x32_bf16 v[58:61], v[180:183], v[220:223], v[58:61]
	v_mfma_f32_16x16x32_bf16 v[106:109], v[184:187], v[192:195], v[90:93]
	v_mfma_f32_16x16x32_bf16 v[86:89], v[150:153], v[204:207], v[86:89]
	v_mfma_f32_16x16x32_bf16 v[82:85], v[184:187], v[204:207], v[82:85]
	v_mfma_f32_16x16x32_bf16 v[78:81], v[150:153], v[216:219], v[78:81]
	v_mfma_f32_16x16x32_bf16 v[74:77], v[184:187], v[216:219], v[74:77]
	v_mfma_f32_16x16x32_bf16 v[62:65], v[150:153], v[224:227], v[62:65]
	v_mfma_f32_16x16x32_bf16 v[58:61], v[184:187], v[224:227], v[58:61]
	s_barrier
	s_setprio 0
	s_add_i32 s65, s65, 2
	s_add_u32 s16, s16, 0x100
	s_addc_u32 s17, s17, 0
	s_add_u32 s41, s41, 0x100
	s_addc_u32 s64, s64, 0
	s_cmp_gt_u32 s65, 29

.LBB0_310:
	s_andn2_b64 vcc, exec, s[4:5]
	s_cbranch_vccnz .LBB0_157
	s_mov_b32 s101, 1
	s_branch .LBB0_157

.LBB0_1328:
	s_mov_b32 s101, 0
	s_mov_b32 s100, 0
	v_readlane_b32 s2, v254, 16
	s_cmp_lt_i32 s2, 8
	v_readlane_b32 s3, v254, 17
	s_cselect_b64 s[4:5], -1, 0
	s_add_u32 s2, s86, 0x4c800000
	s_addc_u32 s3, s87, 0
	s_and_b64 s[0:1], s[4:5], s[0:1]
	s_andn2_b64 vcc, exec, s[0:1]
	s_cbranch_vccnz .LBB0_1353
	v_readlane_b32 s4, v254, 14
	s_cmpk_gt_i32 s4, 0x3ff
	v_readfirstlane_b32 s9, v0
	s_cbranch_scc1 .LBB0_1353
	v_readlane_b32 s5, v254, 14
	s_ashr_i32 s33, s5, 31
	s_lshr_b32 s4, s33, 29
	s_add_i32 s7, s5, s4
	s_and_b32 s4, s7, -8
	s_sub_i32 s8, s5, s4
	s_cmp_gt_i32 s8, -1
	s_cbranch_scc0 .LBB0_1332
	s_lshl_b32 s6, s8, 7
	s_cbranch_execz .LBB0_1333
	s_branch .LBB0_1334

.LBB0_1345:
	s_ashr_i32 s23, s22, 31
	s_lshl_b64 s[24:25], s[22:23], 20
	v_readlane_b32 s26, v254, 22
	v_readlane_b32 s27, v254, 23
	s_add_u32 s24, s26, s24
	s_addc_u32 s25, s27, s25
	s_and_b64 s[26:27], s[8:9], exec
	s_cselect_b32 s23, s25, s31
	s_cselect_b32 s55, s24, s30
	s_ashr_i32 s21, s20, 31
	s_lshl_b64 s[26:27], s[20:21], 20
	s_add_u32 s26, s38, s26
	s_addc_u32 s27, s39, s27
	s_and_b64 s[36:37], s[8:9], exec
	s_cselect_b32 s21, s27, s35
	s_cselect_b32 s56, s26, s34
	s_add_u32 s30, s30, 0x80080
	s_addc_u32 s31, s31, 0
	s_add_u32 s57, s34, 0x100
	s_addc_u32 s58, s35, 0
	s_mov_b32 s59, -2
	s_cmp_lg_u32 s101, 0
	s_cbranch_scc0 .Lbs_1346
	s_barrier
	s_mov_b32 s101, 0
.Lbs_1346:
	ds_read_b128 v[154:157], v150
	ds_read_b128 v[158:161], v150 offset:1024
	ds_read_b128 v[162:165], v150 offset:2048
	ds_read_b128 v[166:169], v150 offset:3072
	ds_read_b128 v[170:173], v151
	ds_read_b128 v[174:177], v151 offset:1024
	ds_read_b128 v[178:181], v151 offset:2048
	ds_read_b128 v[182:185], v151 offset:3072
	s_add_u32 s34, s30, 0xfff80080
	s_addc_u32 s35, s31, -1
	s_cmp_eq_u32 s59, 28
	s_cselect_b32 s37, s23, s35
	s_cselect_b32 s36, s55, s34
	s_cselect_b32 s35, s21, s58
	s_cselect_b32 s34, s56, s57
	v_lshl_add_u64 v[146:147], s[30:31], 0, v[138:139]
	s_add_i32 m0, s29, 0xc000
	ds_read_b128 v[186:189], v152
	ds_read_b128 v[190:193], v152 offset:1024
	ds_read_b128 v[194:197], v152 offset:2048
	ds_read_b128 v[198:201], v152 offset:3072
	ds_read_b128 v[202:205], v152 offset:4096
	ds_read_b128 v[206:209], v152 offset:5120
	ds_read_b128 v[210:213], v152 offset:6144
	ds_read_b128 v[214:217], v152 offset:7168
	global_load_lds_dwordx4 v[146:147], off
	v_lshl_add_u64 v[146:147], s[30:31], 0, v[140:141]
	s_add_i32 m0, s29, 0xe000
	s_nop 0
	global_load_lds_dwordx4 v[146:147], off
	s_cmp_lg_u32 s100, 0
	s_cbranch_scc1 .Lrx_1346_0
	s_waitcnt vmcnt(8)

.LBB0_1349:
	v_lshl_add_u32 v154, s28, 8, v1
	v_lshl_or_b32 v146, s54, 8, v149
	v_ashrrev_i32_e32 v155, 31, v154
	v_ashrrev_i32_e32 v147, 31, v146
	v_lshlrev_b64 v[156:157], 12, v[154:155]
	v_lshl_add_u64 v[156:157], s[2:3], 0, v[156:157]
	v_lshlrev_b64 v[158:159], 1, v[146:147]
	v_lshl_add_u64 v[146:147], v[156:157], 0, v[158:159]
	v_cvt_pk_bf16_f32 v126, v126, v127
	v_cvt_pk_bf16_f32 v127, v128, v129
	v_cvt_pk_bf16_f32 v128, v122, v123
	v_cvt_pk_bf16_f32 v129, v124, v125
	global_store_dwordx4 v[146:147], v[126:129], off
	v_cvt_pk_bf16_f32 v114, v114, v115
	v_cvt_pk_bf16_f32 v115, v116, v117
	v_cvt_pk_bf16_f32 v116, v106, v107
	v_or_b32_e32 v106, 16, v154
	v_ashrrev_i32_e32 v107, 31, v106
	v_lshlrev_b64 v[106:107], 12, v[106:107]
	v_lshl_add_u64 v[106:107], s[2:3], 0, v[106:107]
	v_cvt_pk_bf16_f32 v117, v108, v109
	global_store_dwordx4 v[146:147], v[114:117], off offset:256
	s_nop 1
	v_lshl_add_u64 v[114:115], v[106:107], 0, v[158:159]
	v_cvt_pk_bf16_f32 v106, v118, v119
	v_cvt_pk_bf16_f32 v107, v120, v121
	v_cvt_pk_bf16_f32 v108, v110, v111
	v_cvt_pk_bf16_f32 v109, v112, v113
	global_store_dwordx4 v[114:115], v[106:109], off
	v_cvt_pk_bf16_f32 v98, v98, v99
	v_cvt_pk_bf16_f32 v99, v100, v101
	v_cvt_pk_bf16_f32 v100, v90, v91
	v_or_b32_e32 v90, 32, v154
	v_ashrrev_i32_e32 v91, 31, v90
	v_lshlrev_b64 v[90:91], 12, v[90:91]
	v_lshl_add_u64 v[90:91], s[2:3], 0, v[90:91]
	v_cvt_pk_bf16_f32 v101, v92, v93
	global_store_dwordx4 v[114:115], v[98:101], off offset:256
	s_nop 1
	v_lshl_add_u64 v[98:99], v[90:91], 0, v[158:159]
	v_cvt_pk_bf16_f32 v90, v102, v103
	v_cvt_pk_bf16_f32 v91, v104, v105
	v_cvt_pk_bf16_f32 v92, v94, v95
	v_cvt_pk_bf16_f32 v93, v96, v97
	global_store_dwordx4 v[98:99], v[90:93], off
	v_cvt_pk_bf16_f32 v82, v82, v83
	v_cvt_pk_bf16_f32 v83, v84, v85
	v_cvt_pk_bf16_f32 v84, v74, v75
	v_or_b32_e32 v74, 48, v154
	v_ashrrev_i32_e32 v75, 31, v74
	v_lshlrev_b64 v[74:75], 12, v[74:75]
	v_lshl_add_u64 v[74:75], s[2:3], 0, v[74:75]
	v_cvt_pk_bf16_f32 v85, v76, v77
	global_store_dwordx4 v[98:99], v[82:85], off offset:256
	s_nop 1
	v_lshl_add_u64 v[82:83], v[74:75], 0, v[158:159]
	v_cvt_pk_bf16_f32 v74, v86, v87
	v_cvt_pk_bf16_f32 v75, v88, v89
	v_cvt_pk_bf16_f32 v76, v78, v79
	v_cvt_pk_bf16_f32 v77, v80, v81
	global_store_dwordx4 v[82:83], v[74:77], off
	v_cvt_pk_bf16_f32 v70, v70, v71
	v_cvt_pk_bf16_f32 v71, v72, v73
	v_cvt_pk_bf16_f32 v72, v66, v67
	v_cvt_pk_bf16_f32 v73, v68, v69
	global_store_dwordx4 v[82:83], v[70:73], off offset:256
	v_cvt_pk_bf16_f32 v62, v62, v63
	v_cvt_pk_bf16_f32 v63, v64, v65
	v_cvt_pk_bf16_f32 v64, v58, v59
	v_add_co_u32_e32 v58, vcc, s50, v146
	v_lshl_add_u64 v[66:67], v[146:147], 0, s[4:5]
	s_nop 0
	v_addc_co_u32_e32 v59, vcc, 0, v147, vcc
	v_cvt_pk_bf16_f32 v65, v60, v61
	global_store_dwordx4 v[58:59], v[62:65], off
	v_cvt_pk_bf16_f32 v50, v50, v51
	v_cvt_pk_bf16_f32 v51, v52, v53
	v_cvt_pk_bf16_f32 v52, v42, v43
	v_cvt_pk_bf16_f32 v53, v44, v45
	global_store_dwordx4 v[66:67], v[50:53], off offset:256
	v_cvt_pk_bf16_f32 v42, v54, v55
	v_cvt_pk_bf16_f32 v43, v56, v57
	v_cvt_pk_bf16_f32 v44, v46, v47
	v_add_co_u32_e32 v46, vcc, s51, v146
	s_nop 0
	v_lshl_add_u64 v[50:51], v[146:147], 0, s[14:15]
	v_addc_co_u32_e32 v47, vcc, 0, v147, vcc
	v_cvt_pk_bf16_f32 v45, v48, v49
	global_store_dwordx4 v[46:47], v[42:45], off
	v_cvt_pk_bf16_f32 v34, v34, v35
	v_cvt_pk_bf16_f32 v35, v36, v37
	v_cvt_pk_bf16_f32 v36, v26, v27
	v_cvt_pk_bf16_f32 v37, v28, v29
	global_store_dwordx4 v[50:51], v[34:37], off offset:256
	v_cvt_pk_bf16_f32 v26, v38, v39
	v_cvt_pk_bf16_f32 v27, v40, v41
	v_cvt_pk_bf16_f32 v28, v30, v31
	v_add_co_u32_e32 v30, vcc, s52, v146
	s_nop 0
	v_lshl_add_u64 v[34:35], v[146:147], 0, s[16:17]
	v_addc_co_u32_e32 v31, vcc, 0, v147, vcc
	v_cvt_pk_bf16_f32 v29, v32, v33
	global_store_dwordx4 v[30:31], v[26:29], off
	v_cvt_pk_bf16_f32 v18, v18, v19
	v_cvt_pk_bf16_f32 v19, v20, v21
	v_cvt_pk_bf16_f32 v20, v10, v11
	v_cvt_pk_bf16_f32 v21, v12, v13
	global_store_dwordx4 v[34:35], v[18:21], off offset:256
	v_cvt_pk_bf16_f32 v10, v22, v23
	v_cvt_pk_bf16_f32 v11, v24, v25
	v_cvt_pk_bf16_f32 v12, v14, v15
	v_add_co_u32_e32 v14, vcc, s53, v146
	s_nop 0
	v_lshl_add_u64 v[18:19], v[146:147], 0, s[18:19]
	v_addc_co_u32_e32 v15, vcc, 0, v147, vcc
	s_andn2_b64 vcc, exec, s[8:9]
	s_mov_b64 s[8:9], -1
	v_cvt_pk_bf16_f32 v13, v16, v17
	global_store_dwordx4 v[14:15], v[10:13], off
	v_cvt_pk_bf16_f32 v6, v6, v7
	v_cvt_pk_bf16_f32 v7, v8, v9
	v_cvt_pk_bf16_f32 v8, v2, v3
	v_cvt_pk_bf16_f32 v9, v4, v5
	global_store_dwordx4 v[18:19], v[6:9], off offset:256
	s_cbranch_vccnz .LBB0_1338
	s_andn2_b64 vcc, exec, s[6:7]
	s_cbranch_vccnz .LBB0_1337
	s_mov_b32 s101, 1
	s_branch .LBB0_1337

.LBB0_1469:
	s_mov_b32 s101, 0
	s_mov_b32 s100, 0
	s_cmp_lt_i32 s78, 10
	s_cselect_b64 s[4:5], -1, 0
	s_add_u32 s20, s86, 0x5b200000
	s_addc_u32 s21, s87, 0
	s_and_b64 s[0:1], s[4:5], s[0:1]
	s_andn2_b64 vcc, exec, s[0:1]
	s_cbranch_vccnz .LBB0_1486
	v_readlane_b32 s4, v254, 14
	s_cmpk_gt_i32 s4, 0x15ff
	v_readfirstlane_b32 s12, v0
	s_cbranch_scc1 .LBB0_1486
	v_lshrrev_b32_e32 v1, 5, v0
	v_lshrrev_b32_e32 v3, 1, v0
	v_and_b32_e32 v1, 4, v1
	v_bfe_u32 v2, v0, 2, 2
	v_and_b32_e32 v13, 24, v3
	v_or3_b32 v1, v1, v2, v13
	v_lshlrev_b32_e32 v2, 4, v0
	v_or_b32_e32 v10, 0x2000, v2
	s_add_u32 s15, s86, 0x2500000
	v_lshrrev_b32_e32 v3, 7, v10
	s_movk_i32 s4, 0x60
	v_readlane_b32 s6, v254, 14
	s_addc_u32 s33, s87, 0
	v_and_or_b32 v4, v3, s4, v1
	v_bfe_u32 v14, v0, 2, 4
	s_movk_i32 s4, 0x70
	s_ashr_i32 s37, s6, 31
	v_and_or_b32 v3, v3, s4, v14
	s_lshr_b32 s4, s37, 29
	s_add_i32 s4, s6, s4
	s_lshr_b32 s10, s12, 6
	s_ashr_i32 s5, s4, 3
	s_and_b32 s4, s4, -8
	s_lshr_b32 s9, s12, 8
	s_lshl_b32 s36, s10, 10
	s_sub_i32 s4, s6, s4
	s_cmp_lt_i32 s4, 0
	s_movk_i32 s38, 0x2c1
	s_cselect_b32 s6, s38, 0x2c0
	s_mul_i32 s4, s4, s6
	s_add_i32 s4, s4, s5
	s_mul_hi_i32 s5, s4, 0x2e8ba2e9
	s_lshr_b32 s6, s5, 31
	s_ashr_i32 s5, s5, 6
	s_add_i32 s5, s5, s6
	s_lshl_b32 s6, s5, 3
	s_mulk_i32 s5, 0x160
	s_sub_i32 s4, s4, s5
	s_sext_i32_i16 s5, s4
	s_bfe_u32 s5, s5, 0x3001c
	s_add_i32 s5, s4, s5
	s_sext_i32_i16 s7, s5
	s_and_b32 s5, s5, 0xfff8
	s_sub_i32 s4, s4, s5
	s_sext_i32_i16 s4, s4
	v_and_b32_e32 v5, 32, v0
	s_lshr_b32 s8, s7, 3
	s_add_i32 s26, s6, s4
	v_bitop3_b32 v11, v2, v5, 48 bitop3:0x6c
	v_and_b32_e32 v12, 64, v0
	s_ashr_i32 s27, s26, 31
	s_bfe_i64 s[6:7], s[8:9], 0x100000
	v_or_b32_e32 v2, v11, v12
	s_lshl_b64 s[4:5], s[26:27], 20
	s_lshl_b64 s[6:7], s[6:7], 20
	v_lshl_or_b32 v132, v3, 12, v2
	v_lshrrev_b32_e32 v3, 3, v0
	s_add_u32 s30, s15, s6
	v_and_or_b32 v1, v3, 32, v1
	s_addc_u32 s31, s33, s7
	s_add_i32 s39, s36, 0
	v_lshl_or_b32 v134, v1, 12, v2
	s_add_i32 m0, s39, 0x10000
	v_lshl_or_b32 v130, v4, 12, v2
	global_load_lds_dwordx4 v134, s[30:31]
	s_add_i32 m0, s39, 0x12000
	s_add_u32 s6, s30, 0x80000
	global_load_lds_dwordx4 v130, s[30:31]
	s_addc_u32 s7, s31, 0
	s_add_i32 m0, s39, 0x14000
	v_and_or_b32 v1, v3, 48, v14
	global_load_lds_dwordx4 v134, s[6:7]
	s_add_i32 m0, s39, 0x16000
	s_add_u32 s28, s20, s4
	s_addc_u32 s29, s21, s5
	s_add_i32 s40, s39, 0x2000
	v_lshl_or_b32 v136, v1, 12, v2
	global_load_lds_dwordx4 v130, s[6:7]
	s_mov_b32 m0, s39
	s_add_u32 s4, s28, 0x80000
	global_load_lds_dwordx4 v136, s[28:29]
	s_mov_b32 m0, s40
	s_addc_u32 s5, s29, 0
	s_add_i32 s41, s39, 0x4000
	global_load_lds_dwordx4 v132, s[28:29]
	s_mov_b32 m0, s41
	s_add_i32 s42, s39, 0x6000
	global_load_lds_dwordx4 v136, s[4:5]
	s_mov_b32 m0, s42
	v_mov_b32_e32 v135, 0
	global_load_lds_dwordx4 v132, s[4:5]
	v_mov_b32_e32 v131, v135
	v_mov_b32_e32 v137, v135
	v_mov_b32_e32 v133, v135
	s_cmp_eq_u32 s9, 1
	s_mov_b32 s43, 0
	v_lshl_add_u64 v[8:9], s[30:31], 0, v[134:135]
	v_lshl_add_u64 v[6:7], s[30:31], 0, v[130:131]
	v_lshl_add_u64 v[2:3], s[28:29], 0, v[136:137]
	s_cselect_b64 s[4:5], -1, 0
	s_cmp_lg_u32 s9, 1
	v_lshl_add_u64 v[4:5], s[28:29], 0, v[132:133]
	s_cbranch_scc1 .LBB0_1473
	s_barrier

.LBB0_1478:
	s_ashr_i32 s19, s18, 31
	s_lshl_b64 s[22:23], s[18:19], 20
	s_add_u32 s22, s20, s22
	s_addc_u32 s23, s21, s23
	s_and_b64 s[24:25], s[8:9], exec
	s_cselect_b32 s19, s23, s29
	s_cselect_b32 s27, s22, s28
	s_ashr_i32 s17, s16, 31
	s_lshl_b64 s[24:25], s[16:17], 20
	s_add_u32 s24, s15, s24
	s_addc_u32 s25, s33, s25
	s_and_b64 s[34:35], s[8:9], exec
	s_cselect_b32 s17, s25, s31
	s_cselect_b32 s51, s24, s30
	s_lshl_b32 s34, s26, 8
	s_ashr_i32 s35, s34, 31
	v_lshl_add_u64 v[238:239], s[34:35], 2, v[138:139]
	global_load_dword v240, v[238:239], off
	global_load_dword v242, v[238:239], off offset:64
	global_load_dword v244, v[238:239], off offset:128
	global_load_dword v246, v[238:239], off offset:192
	global_load_dword v248, v[238:239], off offset:512
	global_load_dword v250, v[238:239], off offset:576
	global_load_dword v252, v[238:239], off offset:640
	global_load_dword v238, v[238:239], off offset:704
	s_add_u32 s28, s28, 0x80080
	s_addc_u32 s29, s29, 0
	s_add_u32 s52, s30, 0x100
	s_addc_u32 s53, s31, 0
	s_mov_b32 s54, -2
	s_cmp_lg_u32 s101, 0
	s_cbranch_scc0 .Lbs_1479
	s_barrier
	s_mov_b32 s101, 0
.Lbs_1479:
	ds_read_b128 v[154:157], v150
	ds_read_b128 v[158:161], v150 offset:1024
	ds_read_b128 v[162:165], v150 offset:2048
	ds_read_b128 v[166:169], v150 offset:3072
	ds_read_b128 v[170:173], v151
	ds_read_b128 v[174:177], v151 offset:1024
	ds_read_b128 v[178:181], v151 offset:2048
	ds_read_b128 v[182:185], v151 offset:3072
	s_add_u32 s30, s28, 0xfff80080
	s_addc_u32 s31, s29, -1
	s_cmp_eq_u32 s54, 28
	s_cselect_b32 s35, s19, s31
	s_cselect_b32 s34, s27, s30
	s_cselect_b32 s31, s17, s53
	s_cselect_b32 s30, s51, s52
	v_lshl_add_u64 v[218:219], s[28:29], 0, v[140:141]
	s_add_i32 m0, s39, 0xc000
	ds_read_b128 v[186:189], v152
	ds_read_b128 v[190:193], v152 offset:1024
	ds_read_b128 v[194:197], v152 offset:2048
	ds_read_b128 v[198:201], v152 offset:3072
	ds_read_b128 v[202:205], v152 offset:4096
	ds_read_b128 v[206:209], v152 offset:5120
	ds_read_b128 v[210:213], v152 offset:6144
	ds_read_b128 v[214:217], v152 offset:7168
	global_load_lds_dwordx4 v[218:219], off
	v_lshl_add_u64 v[218:219], s[28:29], 0, v[142:143]
	s_add_i32 m0, s39, 0xe000
	s_nop 0
	global_load_lds_dwordx4 v[218:219], off
	s_cmp_lg_u32 s100, 0
	s_cbranch_scc1 .Lrx_1479_0
	s_waitcnt vmcnt(8)

.LBB0_1482:
	s_lshl_b32 s26, s26, 8
	s_ashr_i32 s27, s26, 31
	v_lshl_add_u64 v[154:155], s[26:27], 2, v[138:139]
	v_mov_b32_e32 v156, v240
	v_mov_b32_e32 v158, v242
	v_mov_b32_e32 v160, v244
	v_mov_b32_e32 v162, v246
	v_mov_b32_e32 v164, v248
	v_mov_b32_e32 v166, v250
	v_mov_b32_e32 v168, v252
	s_nop 0
	v_mov_b32_e32 v154, v238
	v_lshl_or_b32 v170, s50, 7, v149
	v_add_u32_e32 v153, s26, v1
	v_ashrrev_i32_e32 v171, 31, v170
	s_andn2_b64 vcc, exec, s[8:9]
	s_mov_b64 s[8:9], -1
	v_pk_mul_f32 v[126:127], v[126:127], v[156:157] op_sel_hi:[1,0]
	v_pk_mul_f32 v[128:129], v[128:129], v[156:157] op_sel_hi:[1,0]
	v_pk_mul_f32 v[180:181], v[78:79], v[160:161] op_sel_hi:[1,0]
	v_pk_mul_f32 v[178:179], v[82:83], v[158:159] op_sel_hi:[1,0]
	v_pk_mul_f32 v[78:79], v[44:45], v[164:165] op_sel_hi:[1,0]
	v_pk_mul_f32 v[44:45], v[52:53], v[166:167] op_sel_hi:[1,0]
	v_pk_mul_f32 v[52:53], v[18:19], v[166:167] op_sel_hi:[1,0]
	v_pk_mul_f32 v[18:19], v[126:127], s[14:15] op_sel_hi:[1,0]
	v_pk_mul_f32 v[82:83], v[86:87], v[162:163] op_sel_hi:[1,0]
	v_pk_mul_f32 v[86:87], v[68:69], v[162:163] op_sel_hi:[1,0]
	v_pk_mul_f32 v[68:69], v[34:35], v[164:165] op_sel_hi:[1,0]
	v_pk_mul_f32 v[34:35], v[12:13], v[168:169] op_sel_hi:[1,0]
	v_pk_mul_f32 v[12:13], v[22:23], v[154:155] op_sel_hi:[1,0]
	v_pk_mul_f32 v[22:23], v[128:129], s[14:15] op_sel_hi:[1,0]
	v_exp_f32_e32 v18, v18
	v_exp_f32_e32 v19, v19
	v_exp_f32_e32 v22, v22
	v_exp_f32_e32 v23, v23
	v_pk_mul_f32 v[106:107], v[106:107], v[156:157] op_sel_hi:[1,0]
	v_pk_add_f32 v[18:19], v[18:19], 1.0 op_sel_hi:[1,0]
	v_pk_mul_f32 v[124:125], v[124:125], v[156:157] op_sel_hi:[1,0]
	v_pk_add_f32 v[22:23], v[22:23], 1.0 op_sel_hi:[1,0]
	v_rcp_f32_e32 v18, v18
	v_rcp_f32_e32 v19, v19
	v_rcp_f32_e32 v22, v22
	v_rcp_f32_e32 v23, v23
	v_pk_mul_f32 v[122:123], v[122:123], v[156:157] op_sel_hi:[1,0]
	v_pk_mul_f32 v[108:109], v[108:109], v[156:157] op_sel_hi:[1,0]
	v_pk_mul_f32 v[120:121], v[120:121], v[158:159] op_sel_hi:[1,0]
	v_pk_mul_f32 v[118:119], v[118:119], v[158:159] op_sel_hi:[1,0]
	v_pk_mul_f32 v[116:117], v[116:117], v[158:159] op_sel_hi:[1,0]
	v_pk_mul_f32 v[114:115], v[114:115], v[158:159] op_sel_hi:[1,0]
	v_pk_mul_f32 v[174:175], v[90:91], v[158:159] op_sel_hi:[1,0]
	v_pk_mul_f32 v[176:177], v[92:93], v[158:159] op_sel_hi:[1,0]
	v_pk_mul_f32 v[158:159], v[84:85], v[158:159] op_sel_hi:[1,0]
	v_pk_mul_f32 v[84:85], v[66:67], v[162:163] op_sel_hi:[1,0]
	v_pk_mul_f32 v[66:67], v[58:59], v[164:165] op_sel_hi:[1,0]
	v_pk_mul_f32 v[58:59], v[54:55], v[166:167] op_sel_hi:[1,0]
	v_pk_mul_f32 v[54:55], v[20:21], v[166:167] op_sel_hi:[1,0]
	v_pk_mul_f32 v[20:21], v[40:41], v[168:169] op_sel_hi:[1,0]
	v_pk_mul_f32 v[40:41], v[16:17], v[168:169] op_sel_hi:[1,0]
	v_pk_mul_f32 v[16:17], v[30:31], v[154:155] op_sel_hi:[1,0]
	v_pk_mul_f32 v[30:31], v[126:127], v[106:107]
	v_pk_mul_f32 v[172:173], v[98:99], v[156:157] op_sel_hi:[1,0]
	v_pk_mul_f32 v[156:157], v[100:101], v[156:157] op_sel_hi:[1,0]
	v_pk_mul_f32 v[100:101], v[102:103], v[160:161] op_sel_hi:[1,0]
	v_pk_mul_f32 v[102:103], v[74:75], v[160:161] op_sel_hi:[1,0]
	v_pk_mul_f32 v[92:93], v[94:95], v[162:163] op_sel_hi:[1,0]
	v_pk_mul_f32 v[94:95], v[72:73], v[162:163] op_sel_hi:[1,0]
	v_pk_mul_f32 v[72:73], v[64:65], v[164:165] op_sel_hi:[1,0]
	v_pk_mul_f32 v[74:75], v[62:63], v[164:165] op_sel_hi:[1,0]
	v_pk_mul_f32 v[64:65], v[60:61], v[164:165] op_sel_hi:[1,0]
	v_pk_mul_f32 v[60:61], v[26:27], v[166:167] op_sel_hi:[1,0]
	v_pk_mul_f32 v[62:63], v[28:29], v[166:167] op_sel_hi:[1,0]
	v_pk_mul_f32 v[26:27], v[38:39], v[168:169] op_sel_hi:[1,0]
	v_pk_mul_f32 v[38:39], v[14:15], v[168:169] op_sel_hi:[1,0]
	v_pk_mul_f32 v[28:29], v[10:11], v[168:169] op_sel_hi:[1,0]
	v_pk_mul_f32 v[14:15], v[32:33], v[154:155] op_sel_hi:[1,0]
	v_pk_mul_f32 v[10:11], v[24:25], v[154:155] op_sel_hi:[1,0]
	v_pk_mul_f32 v[24:25], v[128:129], v[108:109]
	v_pk_mul_f32 v[32:33], v[122:123], s[14:15] op_sel_hi:[1,0]
	v_pk_mul_f32 v[18:19], v[30:31], v[18:19]
	v_pk_mul_f32 v[30:31], v[124:125], s[14:15] op_sel_hi:[1,0]
	v_pk_mul_f32 v[22:23], v[24:25], v[22:23]
	v_exp_f32_e32 v24, v32
	v_exp_f32_e32 v25, v33
	v_exp_f32_e32 v30, v30
	v_exp_f32_e32 v31, v31
	v_pk_mul_f32 v[98:99], v[104:105], v[160:161] op_sel_hi:[1,0]
	v_pk_add_f32 v[24:25], v[24:25], 1.0 op_sel_hi:[1,0]
	v_pk_mul_f32 v[104:105], v[76:77], v[160:161] op_sel_hi:[1,0]
	v_pk_add_f32 v[30:31], v[30:31], 1.0 op_sel_hi:[1,0]
	v_rcp_f32_e32 v24, v24
	v_rcp_f32_e32 v25, v25
	v_rcp_f32_e32 v30, v30
	v_rcp_f32_e32 v31, v31
	v_pk_mul_f32 v[76:77], v[42:43], v[164:165] op_sel_hi:[1,0]
	v_pk_mul_f32 v[42:43], v[46:47], v[168:169] op_sel_hi:[1,0]
	v_pk_mul_f32 v[32:33], v[124:125], v[156:157]
	v_pk_mul_f32 v[46:47], v[122:123], v[172:173]
	v_pk_mul_f32 v[90:91], v[96:97], v[162:163] op_sel_hi:[1,0]
	v_pk_mul_f32 v[24:25], v[46:47], v[24:25]
	v_pk_mul_f32 v[46:47], v[32:33], v[30:31]
	v_cvt_pk_bf16_f32 v30, v18, v19
	v_mov_b64_e32 v[18:19], s[6:7]
	v_cvt_pk_bf16_f32 v31, v22, v23
	v_cvt_pk_bf16_f32 v32, v24, v25
	v_mad_i64_i32 v[24:25], s[26:27], v153, s49, v[18:19]
	v_lshlrev_b64 v[22:23], 1, v[170:171]
	v_lshl_add_u64 v[24:25], v[24:25], 0, v[22:23]
	v_cvt_pk_bf16_f32 v33, v46, v47
	global_store_dwordx4 v[24:25], v[30:33], off
	v_pk_mul_f32 v[24:25], v[118:119], s[14:15] op_sel_hi:[1,0]
	v_pk_mul_f32 v[46:47], v[118:119], v[174:175]
	v_pk_mul_f32 v[30:31], v[120:121], s[14:15] op_sel_hi:[1,0]
	v_exp_f32_e32 v24, v24
	v_exp_f32_e32 v30, v30
	v_exp_f32_e32 v31, v31
	v_exp_f32_e32 v25, v25
	v_pk_mul_f32 v[32:33], v[120:121], v[176:177]
	v_pk_mul_f32 v[96:97], v[114:115], v[178:179]
	v_pk_add_f32 v[30:31], v[30:31], 1.0 op_sel_hi:[1,0]
	v_pk_add_f32 v[24:25], v[24:25], 1.0 op_sel_hi:[1,0]
	v_rcp_f32_e32 v30, v30
	v_rcp_f32_e32 v31, v31
	v_rcp_f32_e32 v24, v24
	v_rcp_f32_e32 v25, v25
	v_pk_mul_f32 v[112:113], v[112:113], v[160:161] op_sel_hi:[1,0]
	v_pk_mul_f32 v[32:33], v[32:33], v[30:31]
	v_pk_mul_f32 v[30:31], v[114:115], s[14:15] op_sel_hi:[1,0]
	v_pk_mul_f32 v[24:25], v[46:47], v[24:25]
	v_exp_f32_e32 v30, v30
	v_exp_f32_e32 v31, v31
	v_pk_mul_f32 v[46:47], v[116:117], s[14:15] op_sel_hi:[1,0]
	v_pk_mul_f32 v[182:183], v[80:81], v[160:161] op_sel_hi:[1,0]
	v_exp_f32_e32 v46, v46
	v_exp_f32_e32 v47, v47
	v_pk_add_f32 v[30:31], v[30:31], 1.0 op_sel_hi:[1,0]
	v_pk_mul_f32 v[80:81], v[88:89], v[162:163] op_sel_hi:[1,0]
	v_rcp_f32_e32 v30, v30
	v_rcp_f32_e32 v31, v31
	v_pk_add_f32 v[46:47], v[46:47], 1.0 op_sel_hi:[1,0]
	v_pk_mul_f32 v[88:89], v[70:71], v[162:163] op_sel_hi:[1,0]
	v_rcp_f32_e32 v46, v46
	v_rcp_f32_e32 v47, v47
	v_pk_mul_f32 v[96:97], v[96:97], v[30:31]
	v_cvt_pk_bf16_f32 v30, v24, v25
	v_or_b32_e32 v24, 16, v153
	v_mad_i64_i32 v[24:25], s[26:27], v24, s49, v[18:19]
	v_pk_mul_f32 v[70:71], v[36:37], v[164:165] op_sel_hi:[1,0]
	v_pk_mul_f32 v[36:37], v[48:49], v[168:169] op_sel_hi:[1,0]
	v_pk_mul_f32 v[48:49], v[116:117], v[158:159]
	v_cvt_pk_bf16_f32 v31, v32, v33
	v_lshl_add_u64 v[24:25], v[24:25], 0, v[22:23]
	v_pk_mul_f32 v[46:47], v[48:49], v[46:47]
	v_cvt_pk_bf16_f32 v32, v96, v97
	v_pk_mul_f32 v[110:111], v[110:111], v[160:161] op_sel_hi:[1,0]
	v_cvt_pk_bf16_f32 v33, v46, v47
	global_store_dwordx4 v[24:25], v[30:33], off
	v_pk_mul_f32 v[24:25], v[110:111], s[14:15] op_sel_hi:[1,0]
	v_pk_mul_f32 v[46:47], v[110:111], v[180:181]
	v_pk_mul_f32 v[30:31], v[112:113], s[14:15] op_sel_hi:[1,0]
	v_exp_f32_e32 v24, v24
	v_exp_f32_e32 v30, v30
	v_exp_f32_e32 v31, v31
	v_exp_f32_e32 v25, v25
	v_pk_mul_f32 v[32:33], v[112:113], v[182:183]
	v_pk_mul_f32 v[96:97], v[100:101], v[102:103]
	v_pk_add_f32 v[30:31], v[30:31], 1.0 op_sel_hi:[1,0]
	v_pk_add_f32 v[24:25], v[24:25], 1.0 op_sel_hi:[1,0]
	v_rcp_f32_e32 v30, v30
	v_rcp_f32_e32 v31, v31
	v_rcp_f32_e32 v24, v24
	v_rcp_f32_e32 v25, v25
	v_pk_mul_f32 v[48:49], v[98:99], v[104:105]
	v_pk_mul_f32 v[32:33], v[32:33], v[30:31]
	v_pk_mul_f32 v[30:31], v[100:101], s[14:15] op_sel_hi:[1,0]
	v_pk_mul_f32 v[24:25], v[46:47], v[24:25]
	v_exp_f32_e32 v30, v30
	v_exp_f32_e32 v31, v31
	v_pk_mul_f32 v[46:47], v[98:99], s[14:15] op_sel_hi:[1,0]
	v_pk_mul_f32 v[56:57], v[56:57], v[166:167] op_sel_hi:[1,0]
	v_exp_f32_e32 v46, v46
	v_exp_f32_e32 v47, v47
	v_pk_add_f32 v[30:31], v[30:31], 1.0 op_sel_hi:[1,0]
	v_pk_mul_f32 v[50:51], v[50:51], v[166:167] op_sel_hi:[1,0]
	v_rcp_f32_e32 v30, v30
	v_rcp_f32_e32 v31, v31
	v_pk_add_f32 v[46:47], v[46:47], 1.0 op_sel_hi:[1,0]
	v_pk_mul_f32 v[8:9], v[8:9], v[154:155] op_sel_hi:[1,0]
	v_rcp_f32_e32 v46, v46
	v_rcp_f32_e32 v47, v47
	v_pk_mul_f32 v[96:97], v[96:97], v[30:31]
	v_cvt_pk_bf16_f32 v30, v24, v25
	v_or_b32_e32 v24, 32, v153
	v_mad_i64_i32 v[24:25], s[26:27], v24, s49, v[18:19]
	v_cvt_pk_bf16_f32 v31, v32, v33
	v_lshl_add_u64 v[24:25], v[24:25], 0, v[22:23]
	v_pk_mul_f32 v[46:47], v[48:49], v[46:47]
	v_cvt_pk_bf16_f32 v32, v96, v97
	v_pk_mul_f32 v[48:49], v[80:81], v[86:87]
	v_cvt_pk_bf16_f32 v33, v46, v47
	global_store_dwordx4 v[24:25], v[30:33], off
	v_pk_mul_f32 v[24:25], v[92:93], s[14:15] op_sel_hi:[1,0]
	v_pk_mul_f32 v[46:47], v[92:93], v[88:89]
	v_pk_mul_f32 v[30:31], v[90:91], s[14:15] op_sel_hi:[1,0]
	v_exp_f32_e32 v24, v24
	v_exp_f32_e32 v30, v30
	v_exp_f32_e32 v31, v31
	v_exp_f32_e32 v25, v25
	v_pk_mul_f32 v[32:33], v[90:91], v[94:95]
	v_pk_mul_f32 v[8:9], v[14:15], v[8:9]
	v_pk_add_f32 v[30:31], v[30:31], 1.0 op_sel_hi:[1,0]
	v_pk_add_f32 v[24:25], v[24:25], 1.0 op_sel_hi:[1,0]
	v_rcp_f32_e32 v30, v30
	v_rcp_f32_e32 v31, v31
	v_rcp_f32_e32 v24, v24
	v_rcp_f32_e32 v25, v25
	v_pk_mul_f32 v[6:7], v[6:7], v[154:155] op_sel_hi:[1,0]
	v_pk_mul_f32 v[32:33], v[32:33], v[30:31]
	v_pk_mul_f32 v[30:31], v[82:83], s[14:15] op_sel_hi:[1,0]
	v_pk_mul_f32 v[24:25], v[46:47], v[24:25]
	v_exp_f32_e32 v30, v30
	v_exp_f32_e32 v31, v31
	v_pk_mul_f32 v[46:47], v[80:81], s[14:15] op_sel_hi:[1,0]
	v_pk_mul_f32 v[80:81], v[82:83], v[84:85]
	v_exp_f32_e32 v46, v46
	v_exp_f32_e32 v47, v47
	v_pk_add_f32 v[30:31], v[30:31], 1.0 op_sel_hi:[1,0]
	v_pk_mul_f32 v[6:7], v[16:17], v[6:7]
	v_rcp_f32_e32 v30, v30
	v_rcp_f32_e32 v31, v31
	v_pk_add_f32 v[46:47], v[46:47], 1.0 op_sel_hi:[1,0]
	v_pk_mul_f32 v[2:3], v[2:3], v[154:155] op_sel_hi:[1,0]
	v_rcp_f32_e32 v46, v46
	v_rcp_f32_e32 v47, v47
	v_pk_mul_f32 v[80:81], v[80:81], v[30:31]
	v_cvt_pk_bf16_f32 v30, v24, v25
	v_or_b32_e32 v24, 48, v153
	v_mad_i64_i32 v[24:25], s[26:27], v24, s49, v[18:19]
	v_cvt_pk_bf16_f32 v31, v32, v33
	v_lshl_add_u64 v[24:25], v[24:25], 0, v[22:23]
	v_pk_mul_f32 v[46:47], v[48:49], v[46:47]
	v_cvt_pk_bf16_f32 v32, v80, v81
	v_add_u32_e32 v80, 0x80, v153
	v_cvt_pk_bf16_f32 v33, v46, v47
	global_store_dwordx4 v[24:25], v[30:33], off
	v_pk_mul_f32 v[24:25], v[74:75], s[14:15] op_sel_hi:[1,0]
	v_pk_mul_f32 v[46:47], v[74:75], v[76:77]
	v_pk_mul_f32 v[30:31], v[72:73], s[14:15] op_sel_hi:[1,0]
	v_exp_f32_e32 v24, v24
	v_exp_f32_e32 v30, v30
	v_exp_f32_e32 v31, v31
	v_exp_f32_e32 v25, v25
	v_pk_mul_f32 v[32:33], v[72:73], v[78:79]
	v_pk_mul_f32 v[48:49], v[64:65], v[70:71]
	v_pk_add_f32 v[30:31], v[30:31], 1.0 op_sel_hi:[1,0]
	v_pk_add_f32 v[24:25], v[24:25], 1.0 op_sel_hi:[1,0]
	v_rcp_f32_e32 v30, v30
	v_rcp_f32_e32 v31, v31
	v_rcp_f32_e32 v24, v24
	v_rcp_f32_e32 v25, v25
	v_pk_mul_f32 v[4:5], v[4:5], v[154:155] op_sel_hi:[1,0]
	v_pk_mul_f32 v[32:33], v[32:33], v[30:31]
	v_pk_mul_f32 v[30:31], v[66:67], s[14:15] op_sel_hi:[1,0]
	v_pk_mul_f32 v[24:25], v[46:47], v[24:25]
	v_exp_f32_e32 v30, v30
	v_exp_f32_e32 v31, v31
	v_pk_mul_f32 v[46:47], v[64:65], s[14:15] op_sel_hi:[1,0]
	v_pk_mul_f32 v[64:65], v[66:67], v[68:69]
	v_exp_f32_e32 v46, v46
	v_exp_f32_e32 v47, v47
	v_pk_add_f32 v[30:31], v[30:31], 1.0 op_sel_hi:[1,0]
	v_pk_mul_f32 v[2:3], v[12:13], v[2:3]
	v_rcp_f32_e32 v30, v30
	v_rcp_f32_e32 v31, v31
	v_pk_add_f32 v[46:47], v[46:47], 1.0 op_sel_hi:[1,0]
	v_pk_mul_f32 v[4:5], v[10:11], v[4:5]
	v_rcp_f32_e32 v46, v46
	v_rcp_f32_e32 v47, v47
	v_pk_mul_f32 v[64:65], v[64:65], v[30:31]
	v_cvt_pk_bf16_f32 v30, v24, v25
	v_mad_i64_i32 v[24:25], s[26:27], v80, s49, v[18:19]
	v_cvt_pk_bf16_f32 v31, v32, v33
	v_lshl_add_u64 v[24:25], v[24:25], 0, v[22:23]
	v_pk_mul_f32 v[46:47], v[48:49], v[46:47]
	v_cvt_pk_bf16_f32 v32, v64, v65
	v_pk_mul_f32 v[48:49], v[50:51], v[52:53]
	v_cvt_pk_bf16_f32 v33, v46, v47
	global_store_dwordx4 v[24:25], v[30:33], off
	v_pk_mul_f32 v[24:25], v[58:59], s[14:15] op_sel_hi:[1,0]
	v_pk_mul_f32 v[46:47], v[58:59], v[60:61]
	v_pk_mul_f32 v[30:31], v[56:57], s[14:15] op_sel_hi:[1,0]
	v_exp_f32_e32 v24, v24
	v_exp_f32_e32 v30, v30
	v_exp_f32_e32 v31, v31
	v_exp_f32_e32 v25, v25
	v_pk_mul_f32 v[32:33], v[56:57], v[62:63]
	v_pk_add_f32 v[30:31], v[30:31], 1.0 op_sel_hi:[1,0]
	s_nop 0
	v_rcp_f32_e32 v30, v30
	v_rcp_f32_e32 v31, v31
	v_pk_add_f32 v[24:25], v[24:25], 1.0 op_sel_hi:[1,0]
	v_pk_mul_f32 v[32:33], v[32:33], v[30:31]
	v_rcp_f32_e32 v24, v24
	v_rcp_f32_e32 v25, v25
	v_pk_mul_f32 v[30:31], v[50:51], s[14:15] op_sel_hi:[1,0]
	v_pk_mul_f32 v[24:25], v[46:47], v[24:25]
	v_exp_f32_e32 v30, v30
	v_exp_f32_e32 v31, v31
	v_pk_mul_f32 v[46:47], v[44:45], s[14:15] op_sel_hi:[1,0]
	v_pk_mul_f32 v[44:45], v[44:45], v[54:55]
	v_exp_f32_e32 v46, v46
	v_exp_f32_e32 v47, v47
	v_pk_add_f32 v[30:31], v[30:31], 1.0 op_sel_hi:[1,0]
	v_pk_add_f32 v[46:47], v[46:47], 1.0 op_sel_hi:[1,0]
	v_rcp_f32_e32 v30, v30
	v_rcp_f32_e32 v31, v31
	v_rcp_f32_e32 v46, v46
	v_rcp_f32_e32 v47, v47
	v_pk_mul_f32 v[48:49], v[48:49], v[30:31]
	v_cvt_pk_bf16_f32 v30, v24, v25
	v_add_u32_e32 v24, 0x90, v153
	v_mad_i64_i32 v[24:25], s[26:27], v24, s49, v[18:19]
	v_cvt_pk_bf16_f32 v31, v32, v33
	v_lshl_add_u64 v[24:25], v[24:25], 0, v[22:23]
	v_pk_mul_f32 v[44:45], v[44:45], v[46:47]
	v_cvt_pk_bf16_f32 v32, v48, v49
	s_nop 0
	v_cvt_pk_bf16_f32 v33, v44, v45
	global_store_dwordx4 v[24:25], v[30:33], off
	v_pk_mul_f32 v[24:25], v[42:43], s[14:15] op_sel_hi:[1,0]
	s_nop 0
	v_pk_mul_f32 v[30:31], v[36:37], s[14:15] op_sel_hi:[1,0]
	v_exp_f32_e32 v24, v24
	v_exp_f32_e32 v25, v25
	v_exp_f32_e32 v30, v30
	v_exp_f32_e32 v31, v31
	v_pk_mul_f32 v[32:33], v[36:37], v[40:41]
	v_pk_add_f32 v[24:25], v[24:25], 1.0 op_sel_hi:[1,0]
	v_pk_mul_f32 v[36:37], v[42:43], v[38:39]
	v_pk_add_f32 v[30:31], v[30:31], 1.0 op_sel_hi:[1,0]
	v_rcp_f32_e32 v24, v24
	v_rcp_f32_e32 v25, v25
	v_rcp_f32_e32 v30, v30
	v_rcp_f32_e32 v31, v31
	v_pk_mul_f32 v[24:25], v[36:37], v[24:25]
	v_pk_mul_f32 v[36:37], v[20:21], s[14:15] op_sel_hi:[1,0]
	v_pk_mul_f32 v[30:31], v[32:33], v[30:31]
	v_pk_mul_f32 v[32:33], v[26:27], s[14:15] op_sel_hi:[1,0]
	v_exp_f32_e32 v36, v36
	v_exp_f32_e32 v32, v32
	v_exp_f32_e32 v33, v33
	v_exp_f32_e32 v37, v37
	v_pk_mul_f32 v[20:21], v[20:21], v[34:35]
	v_pk_mul_f32 v[26:27], v[26:27], v[28:29]
	v_pk_add_f32 v[32:33], v[32:33], 1.0 op_sel_hi:[1,0]
	v_pk_add_f32 v[36:37], v[36:37], 1.0 op_sel_hi:[1,0]
	v_rcp_f32_e32 v32, v32
	v_rcp_f32_e32 v33, v33
	v_rcp_f32_e32 v36, v36
	v_rcp_f32_e32 v37, v37
	v_cvt_pk_bf16_f32 v24, v24, v25
	v_pk_mul_f32 v[26:27], v[26:27], v[32:33]
	v_cvt_pk_bf16_f32 v25, v30, v31
	v_pk_mul_f32 v[20:21], v[20:21], v[36:37]
	v_cvt_pk_bf16_f32 v26, v26, v27
	s_nop 0
	v_cvt_pk_bf16_f32 v27, v20, v21
	v_add_u32_e32 v20, 0xa0, v153
	v_mad_i64_i32 v[20:21], s[26:27], v20, s49, v[18:19]
	v_lshl_add_u64 v[20:21], v[20:21], 0, v[22:23]
	global_store_dwordx4 v[20:21], v[24:27], off
	v_pk_mul_f32 v[20:21], v[16:17], s[14:15] op_sel_hi:[1,0]
	v_pk_mul_f32 v[16:17], v[10:11], s[14:15] op_sel_hi:[1,0]
	v_exp_f32_e32 v20, v20
	v_exp_f32_e32 v21, v21
	v_pk_mul_f32 v[24:25], v[14:15], s[14:15] op_sel_hi:[1,0]
	v_pk_mul_f32 v[14:15], v[12:13], s[14:15] op_sel_hi:[1,0]
	v_exp_f32_e32 v24, v24
	v_exp_f32_e32 v14, v14
	v_exp_f32_e32 v15, v15
	v_exp_f32_e32 v25, v25
	v_pk_add_f32 v[20:21], v[20:21], 1.0 op_sel_hi:[1,0]
	v_exp_f32_e32 v16, v16
	v_exp_f32_e32 v17, v17
	v_rcp_f32_e32 v20, v20
	v_rcp_f32_e32 v21, v21
	v_pk_add_f32 v[14:15], v[14:15], 1.0 op_sel_hi:[1,0]
	v_pk_add_f32 v[24:25], v[24:25], 1.0 op_sel_hi:[1,0]
	v_rcp_f32_e32 v14, v14
	v_rcp_f32_e32 v15, v15
	v_pk_add_f32 v[16:17], v[16:17], 1.0 op_sel_hi:[1,0]
	v_rcp_f32_e32 v24, v24
	v_rcp_f32_e32 v25, v25
	v_pk_mul_f32 v[6:7], v[6:7], v[20:21]
	v_rcp_f32_e32 v16, v16
	v_rcp_f32_e32 v17, v17
	v_pk_mul_f32 v[10:11], v[2:3], v[14:15]
	v_cvt_pk_bf16_f32 v2, v6, v7
	v_add_u32_e32 v6, 0xb0, v153
	v_mad_i64_i32 v[6:7], s[26:27], v6, s49, v[18:19]
	v_lshl_add_u64 v[6:7], v[6:7], 0, v[22:23]
	v_pk_mul_f32 v[8:9], v[8:9], v[24:25]
	v_pk_mul_f32 v[12:13], v[4:5], v[16:17]
	v_cvt_pk_bf16_f32 v3, v8, v9
	v_cvt_pk_bf16_f32 v4, v10, v11
	s_nop 0
	v_cvt_pk_bf16_f32 v5, v12, v13
	global_store_dwordx4 v[6:7], v[2:5], off
	s_cbranch_vccnz .LBB0_1475
	s_andn2_b64 vcc, exec, s[4:5]
	s_cbranch_vccnz .LBB0_1474
	s_mov_b32 s101, 1
	s_branch .LBB0_1474

.LBB0_1540:
	s_mov_b32 s101, 0
	s_mov_b32 s100, 0
	s_cmp_lt_i32 s78, 11
	s_cselect_b64 s[0:1], -1, 0
	s_and_b64 s[4:5], s[0:1], s[4:5]
	s_andn2_b64 vcc, exec, s[4:5]
	s_cbranch_vccnz .LBB0_1569
	v_readlane_b32 s0, v254, 14
	s_cmpk_gt_i32 s0, 0x3ff
	v_readfirstlane_b32 s8, v0
	s_cbranch_scc1 .LBB0_1569
	v_readlane_b32 s1, v254, 14
	s_ashr_i32 s33, s1, 31
	s_lshr_b32 s0, s33, 29
	s_add_i32 s7, s1, s0
	s_and_b32 s0, s7, -8
	s_sub_i32 s9, s1, s0
	s_cmp_gt_i32 s9, -1
	s_cbranch_scc0 .LBB0_1544
	s_lshl_b32 s6, s9, 7
	s_cbranch_execz .LBB0_1545
	s_branch .LBB0_1546

.LBB0_1561:
	s_add_u32 s26, s26, 0x160080
	s_addc_u32 s27, s27, 0
	s_add_u32 s57, s28, 0x100
	s_addc_u32 s58, s29, 0
	s_mov_b32 s59, -2
	s_cmp_lg_u32 s101, 0
	s_cbranch_scc0 .Lbs_1562
	s_barrier
	s_mov_b32 s101, 0
.Lbs_1562:
	ds_read_b128 v[154:157], v150
	ds_read_b128 v[158:161], v150 offset:1024
	ds_read_b128 v[162:165], v150 offset:2048
	ds_read_b128 v[166:169], v150 offset:3072
	ds_read_b128 v[170:173], v151
	ds_read_b128 v[174:177], v151 offset:1024
	ds_read_b128 v[178:181], v151 offset:2048
	ds_read_b128 v[182:185], v151 offset:3072
	s_add_u32 s28, s26, 0xffea0080
	s_addc_u32 s29, s27, -1
	s_cmpk_eq_i32 s59, 0x54
	s_cselect_b32 s31, s1, s29
	s_cselect_b32 s30, s0, s28
	s_cselect_b32 s29, s25, s58
	s_cselect_b32 s28, s24, s57
	v_lshl_add_u64 v[146:147], s[26:27], 0, v[138:139]
	s_add_i32 m0, s39, 0xc000
	ds_read_b128 v[186:189], v152
	ds_read_b128 v[190:193], v152 offset:1024
	ds_read_b128 v[194:197], v152 offset:2048
	ds_read_b128 v[198:201], v152 offset:3072
	ds_read_b128 v[202:205], v152 offset:4096
	ds_read_b128 v[206:209], v152 offset:5120
	ds_read_b128 v[210:213], v152 offset:6144
	ds_read_b128 v[214:217], v152 offset:7168
	global_load_lds_dwordx4 v[146:147], off
	v_lshl_add_u64 v[146:147], s[26:27], 0, v[140:141]
	s_add_i32 m0, s39, 0xe000
	s_nop 0
	global_load_lds_dwordx4 v[146:147], off
	s_cmp_lg_u32 s100, 0
	s_cbranch_scc1 .Lrx_1562_0
	s_waitcnt vmcnt(8)

.LBB0_1565:
	v_lshl_add_u32 v154, s55, 8, v1
	v_lshl_or_b32 v146, s56, 8, v149
	v_ashrrev_i32_e32 v155, 31, v154
	v_ashrrev_i32_e32 v147, 31, v146
	v_lshlrev_b64 v[156:157], 12, v[154:155]
	v_lshl_add_u64 v[156:157], s[2:3], 0, v[156:157]
	v_lshlrev_b64 v[158:159], 1, v[146:147]
	v_lshl_add_u64 v[146:147], v[156:157], 0, v[158:159]
	v_cvt_pk_bf16_f32 v126, v126, v127
	v_cvt_pk_bf16_f32 v127, v128, v129
	v_cvt_pk_bf16_f32 v128, v122, v123
	v_cvt_pk_bf16_f32 v129, v124, v125
	global_store_dwordx4 v[146:147], v[126:129], off
	v_cvt_pk_bf16_f32 v114, v114, v115
	v_cvt_pk_bf16_f32 v115, v116, v117
	v_cvt_pk_bf16_f32 v116, v106, v107
	v_or_b32_e32 v106, 16, v154
	v_ashrrev_i32_e32 v107, 31, v106
	v_lshlrev_b64 v[106:107], 12, v[106:107]
	v_lshl_add_u64 v[106:107], s[2:3], 0, v[106:107]
	v_cvt_pk_bf16_f32 v117, v108, v109
	global_store_dwordx4 v[146:147], v[114:117], off offset:256
	s_nop 1
	v_lshl_add_u64 v[114:115], v[106:107], 0, v[158:159]
	v_cvt_pk_bf16_f32 v106, v118, v119
	v_cvt_pk_bf16_f32 v107, v120, v121
	v_cvt_pk_bf16_f32 v108, v110, v111
	v_cvt_pk_bf16_f32 v109, v112, v113
	global_store_dwordx4 v[114:115], v[106:109], off
	v_cvt_pk_bf16_f32 v98, v98, v99
	v_cvt_pk_bf16_f32 v99, v100, v101
	v_cvt_pk_bf16_f32 v100, v90, v91
	v_or_b32_e32 v90, 32, v154
	v_ashrrev_i32_e32 v91, 31, v90
	v_lshlrev_b64 v[90:91], 12, v[90:91]
	v_lshl_add_u64 v[90:91], s[2:3], 0, v[90:91]
	v_cvt_pk_bf16_f32 v101, v92, v93
	global_store_dwordx4 v[114:115], v[98:101], off offset:256
	s_nop 1
	v_lshl_add_u64 v[98:99], v[90:91], 0, v[158:159]
	v_cvt_pk_bf16_f32 v90, v102, v103
	v_cvt_pk_bf16_f32 v91, v104, v105
	v_cvt_pk_bf16_f32 v92, v94, v95
	v_cvt_pk_bf16_f32 v93, v96, v97
	global_store_dwordx4 v[98:99], v[90:93], off
	v_cvt_pk_bf16_f32 v82, v82, v83
	v_cvt_pk_bf16_f32 v83, v84, v85
	v_cvt_pk_bf16_f32 v84, v74, v75
	v_or_b32_e32 v74, 48, v154
	v_ashrrev_i32_e32 v75, 31, v74
	v_lshlrev_b64 v[74:75], 12, v[74:75]
	v_lshl_add_u64 v[74:75], s[2:3], 0, v[74:75]
	v_cvt_pk_bf16_f32 v85, v76, v77
	global_store_dwordx4 v[98:99], v[82:85], off offset:256
	s_nop 1
	v_lshl_add_u64 v[82:83], v[74:75], 0, v[158:159]
	v_cvt_pk_bf16_f32 v74, v86, v87
	v_cvt_pk_bf16_f32 v75, v88, v89
	v_cvt_pk_bf16_f32 v76, v78, v79
	v_cvt_pk_bf16_f32 v77, v80, v81
	global_store_dwordx4 v[82:83], v[74:77], off
	v_cvt_pk_bf16_f32 v70, v70, v71
	v_cvt_pk_bf16_f32 v71, v72, v73
	v_cvt_pk_bf16_f32 v72, v66, v67
	v_cvt_pk_bf16_f32 v73, v68, v69
	global_store_dwordx4 v[82:83], v[70:73], off offset:256
	v_cvt_pk_bf16_f32 v62, v62, v63
	v_cvt_pk_bf16_f32 v63, v64, v65
	v_cvt_pk_bf16_f32 v64, v58, v59
	v_add_co_u32_e32 v58, vcc, s49, v146
	v_lshl_add_u64 v[66:67], v[146:147], 0, s[14:15]
	s_nop 0
	v_addc_co_u32_e32 v59, vcc, 0, v147, vcc
	v_cvt_pk_bf16_f32 v65, v60, v61
	global_store_dwordx4 v[58:59], v[62:65], off
	v_cvt_pk_bf16_f32 v50, v50, v51
	v_cvt_pk_bf16_f32 v51, v52, v53
	v_cvt_pk_bf16_f32 v52, v42, v43
	v_cvt_pk_bf16_f32 v53, v44, v45
	global_store_dwordx4 v[66:67], v[50:53], off offset:256
	v_cvt_pk_bf16_f32 v42, v54, v55
	v_cvt_pk_bf16_f32 v43, v56, v57
	v_cvt_pk_bf16_f32 v44, v46, v47
	v_add_co_u32_e32 v46, vcc, s50, v146
	s_nop 0
	v_lshl_add_u64 v[50:51], v[146:147], 0, s[16:17]
	v_addc_co_u32_e32 v47, vcc, 0, v147, vcc
	v_cvt_pk_bf16_f32 v45, v48, v49
	global_store_dwordx4 v[46:47], v[42:45], off
	v_cvt_pk_bf16_f32 v34, v34, v35
	v_cvt_pk_bf16_f32 v35, v36, v37
	v_cvt_pk_bf16_f32 v36, v26, v27
	v_cvt_pk_bf16_f32 v37, v28, v29
	global_store_dwordx4 v[50:51], v[34:37], off offset:256
	v_cvt_pk_bf16_f32 v26, v38, v39
	v_cvt_pk_bf16_f32 v27, v40, v41
	v_cvt_pk_bf16_f32 v28, v30, v31
	v_add_co_u32_e32 v30, vcc, s51, v146
	s_nop 0
	v_lshl_add_u64 v[34:35], v[146:147], 0, s[18:19]
	v_addc_co_u32_e32 v31, vcc, 0, v147, vcc
	v_cvt_pk_bf16_f32 v29, v32, v33
	global_store_dwordx4 v[30:31], v[26:29], off
	v_cvt_pk_bf16_f32 v18, v18, v19
	v_cvt_pk_bf16_f32 v19, v20, v21
	v_cvt_pk_bf16_f32 v20, v10, v11
	v_cvt_pk_bf16_f32 v21, v12, v13
	global_store_dwordx4 v[34:35], v[18:21], off offset:256
	v_cvt_pk_bf16_f32 v10, v22, v23
	v_cvt_pk_bf16_f32 v11, v24, v25
	v_cvt_pk_bf16_f32 v12, v14, v15
	v_add_co_u32_e32 v14, vcc, s52, v146
	s_nop 0
	v_lshl_add_u64 v[18:19], v[146:147], 0, s[22:23]
	v_addc_co_u32_e32 v15, vcc, 0, v147, vcc
	s_and_b64 vcc, exec, s[8:9]
	s_mov_b64 s[8:9], -1
	v_cvt_pk_bf16_f32 v13, v16, v17
	global_store_dwordx4 v[14:15], v[10:13], off
	v_cvt_pk_bf16_f32 v6, v6, v7
	v_cvt_pk_bf16_f32 v7, v8, v9
	v_cvt_pk_bf16_f32 v8, v2, v3
	v_cvt_pk_bf16_f32 v9, v4, v5
	global_store_dwordx4 v[18:19], v[6:9], off offset:256
	s_cbranch_vccnz .LBB0_1550
	s_andn2_b64 vcc, exec, s[6:7]
	s_cbranch_vccnz .LBB0_1549
	s_mov_b32 s101, 1
	s_branch .LBB0_1549

.LBB0_1685:
	s_mov_b32 s101, 0
	s_cmp_lt_i32 s78, 13
	s_cselect_b64 s[4:5], -1, 0
	s_and_b64 s[0:1], s[4:5], s[0:1]
	s_andn2_b64 vcc, exec, s[0:1]
	s_cbranch_vccnz .LBB0_1729
	v_readlane_b32 s6, v254, 14
	s_cmpk_lt_i32 s6, 0xc80
	s_cselect_b64 s[4:5], -1, 0
	s_cmpk_gt_i32 s6, 0xc7f
	v_readfirstlane_b32 s8, v0
	s_cbranch_scc1 .LBB0_1688
	v_readlane_b32 s9, v254, 14
	s_ashr_i32 s6, s9, 31
	s_lshr_b32 s6, s6, 29
	s_add_i32 s6, s9, s6
	s_ashr_i32 s7, s6, 3
	s_and_b32 s6, s6, -8
	s_sub_i32 s6, s9, s6
	s_cmp_lt_i32 s6, 0
	s_movk_i32 s9, 0x191
	s_cselect_b32 s9, s9, 0x190
	s_mul_i32 s6, s6, s9
	s_add_i32 s6, s6, s7
	s_mul_hi_i32 s7, s6, 0x51eb851f
	s_lshr_b32 s9, s7, 31
	s_ashr_i32 s7, s7, 6
	s_add_i32 s7, s7, s9
	s_lshl_b32 s9, s7, 3
	s_mulk_i32 s7, 0xc8
	s_sub_i32 s6, s6, s7
	s_sext_i32_i16 s7, s6
	s_bfe_u32 s7, s7, 0x3001c
	s_add_i32 s7, s6, s7
	s_sext_i32_i16 s10, s7
	s_and_b32 s7, s7, 0xfff8
	s_sub_i32 s6, s6, s7
	s_sext_i32_i16 s6, s6
	s_add_i32 s44, s9, s6
	s_ashr_i32 s42, s10, 3

.LBB0_1696:
	s_ashr_i32 s37, s36, 31
	s_lshl_b64 s[38:39], s[36:37], 20
	s_add_u32 s38, s20, s38
	s_addc_u32 s39, s21, s39
	s_and_b64 s[40:41], s[10:11], exec
	s_cselect_b32 s37, s39, s47
	s_cselect_b32 s43, s38, s46
	s_ashr_i32 s35, s34, 31
	s_lshl_b64 s[40:41], s[34:35], 20
	s_add_u32 s40, s23, s40
	s_addc_u32 s41, s33, s41
	s_and_b64 s[50:51], s[10:11], exec
	s_cselect_b32 s35, s41, s49
	s_cselect_b32 s45, s40, s48
	s_lshl_b32 s50, s44, 8
	s_ashr_i32 s51, s50, 31
	v_lshl_add_u64 v[238:239], s[50:51], 2, v[140:141]
	global_load_dword v240, v[238:239], off
	global_load_dword v242, v[238:239], off offset:64
	global_load_dword v244, v[238:239], off offset:128
	global_load_dword v246, v[238:239], off offset:192
	global_load_dword v248, v[238:239], off offset:512
	global_load_dword v250, v[238:239], off offset:576
	global_load_dword v252, v[238:239], off offset:640
	global_load_dword v238, v[238:239], off offset:704
	s_add_u32 s46, s46, 0x80080
	s_addc_u32 s47, s47, 0
	s_add_u32 s69, s48, 0x100
	s_addc_u32 s70, s49, 0
	s_mov_b32 s71, -2
	s_waitcnt vmcnt(0)
	s_cmp_lg_u32 s101, 0
	s_cbranch_scc0 .Lbs_1697
	s_barrier
	s_mov_b32 s101, 0
.Lbs_1697:
	ds_read_b128 v[156:159], v176
	ds_read_b128 v[160:163], v176 offset:1024
	ds_read_b128 v[164:167], v176 offset:2048
	ds_read_b128 v[168:171], v176 offset:3072
	ds_read_b128 v[180:183], v177
	ds_read_b128 v[184:187], v177 offset:1024
	ds_read_b128 v[188:191], v177 offset:2048
	ds_read_b128 v[192:195], v177 offset:3072
	s_add_u32 s48, s46, 0xfff80080
	s_addc_u32 s49, s47, -1
	s_cmp_eq_u32 s71, 28
	s_cselect_b32 s51, s37, s49
	s_cselect_b32 s50, s43, s48
	s_cselect_b32 s49, s35, s70
	s_cselect_b32 s48, s45, s69
	v_lshl_add_u64 v[172:173], s[46:47], 0, v[148:149]
	s_add_i32 m0, s53, 0xc000
	ds_read_b128 v[196:199], v178
	ds_read_b128 v[200:203], v178 offset:1024
	ds_read_b128 v[204:207], v178 offset:2048
	ds_read_b128 v[208:211], v178 offset:3072
	ds_read_b128 v[212:215], v178 offset:4096
	ds_read_b128 v[216:219], v178 offset:5120
	ds_read_b128 v[220:223], v178 offset:6144
	ds_read_b128 v[224:227], v178 offset:7168
	global_load_lds_dwordx4 v[172:173], off
	v_lshl_add_u64 v[172:173], s[46:47], 0, v[150:151]
	s_add_i32 m0, s53, 0xe000
	s_nop 0
	global_load_lds_dwordx4 v[172:173], off
	s_waitcnt vmcnt(8)
	s_waitcnt lgkmcnt(0)
	s_setprio 1
	s_barrier
	v_mfma_f32_16x16x32_bf16 v[126:129], v[156:159], v[196:199], 0
	v_mfma_f32_16x16x32_bf16 v[122:125], v[164:167], v[196:199], 0
	v_mfma_f32_16x16x32_bf16 v[118:121], v[156:159], v[204:207], 0
	v_mfma_f32_16x16x32_bf16 v[114:117], v[164:167], v[204:207], 0
	v_mfma_f32_16x16x32_bf16 v[110:113], v[156:159], v[212:215], 0
	v_mfma_f32_16x16x32_bf16 v[106:109], v[164:167], v[212:215], 0
	v_mfma_f32_16x16x32_bf16 v[102:105], v[156:159], v[220:223], 0
	v_mfma_f32_16x16x32_bf16 v[98:101], v[164:167], v[220:223], 0
	v_mfma_f32_16x16x32_bf16 v[126:129], v[160:163], v[200:203], v[126:129]
	v_mfma_f32_16x16x32_bf16 v[122:125], v[168:171], v[200:203], v[122:125]
	v_mfma_f32_16x16x32_bf16 v[118:121], v[160:163], v[208:211], v[118:121]
	v_mfma_f32_16x16x32_bf16 v[114:117], v[168:171], v[208:211], v[114:117]
	v_mfma_f32_16x16x32_bf16 v[110:113], v[160:163], v[216:219], v[110:113]
	v_mfma_f32_16x16x32_bf16 v[106:109], v[168:171], v[216:219], v[106:109]
	v_mfma_f32_16x16x32_bf16 v[102:105], v[160:163], v[224:227], v[102:105]
	v_mfma_f32_16x16x32_bf16 v[98:101], v[168:171], v[224:227], v[98:101]
	s_setprio 0
	s_setprio 1
	v_mfma_f32_16x16x32_bf16 v[38:41], v[180:183], v[196:199], 0
	v_mfma_f32_16x16x32_bf16 v[34:37], v[188:191], v[196:199], 0
	v_mfma_f32_16x16x32_bf16 v[46:49], v[180:183], v[204:207], 0
	v_mfma_f32_16x16x32_bf16 v[42:45], v[188:191], v[204:207], 0
	v_mfma_f32_16x16x32_bf16 v[54:57], v[180:183], v[212:215], 0
	v_mfma_f32_16x16x32_bf16 v[50:53], v[188:191], v[212:215], 0
	v_mfma_f32_16x16x32_bf16 v[62:65], v[180:183], v[220:223], 0
	v_mfma_f32_16x16x32_bf16 v[58:61], v[188:191], v[220:223], 0
	v_mfma_f32_16x16x32_bf16 v[38:41], v[184:187], v[200:203], v[38:41]
	v_mfma_f32_16x16x32_bf16 v[34:37], v[192:195], v[200:203], v[34:37]
	v_mfma_f32_16x16x32_bf16 v[46:49], v[184:187], v[208:211], v[46:49]
	v_mfma_f32_16x16x32_bf16 v[42:45], v[192:195], v[208:211], v[42:45]
	v_mfma_f32_16x16x32_bf16 v[54:57], v[184:187], v[216:219], v[54:57]
	v_mfma_f32_16x16x32_bf16 v[50:53], v[192:195], v[216:219], v[50:53]
	v_mfma_f32_16x16x32_bf16 v[62:65], v[184:187], v[224:227], v[62:65]
	v_mfma_f32_16x16x32_bf16 v[58:61], v[192:195], v[224:227], v[58:61]
	s_barrier
	s_setprio 0
	s_add_i32 s72, s65, s52
	v_lshl_add_u64 v[172:173], s[48:49], 0, v[132:133]
	s_mov_b32 m0, s72
	ds_read_b128 v[196:199], v178 offset:16384
	ds_read_b128 v[200:203], v178 offset:17408
	ds_read_b128 v[204:207], v178 offset:18432
	ds_read_b128 v[208:211], v178 offset:19456
	ds_read_b128 v[212:215], v178 offset:20480
	ds_read_b128 v[216:219], v178 offset:21504
	ds_read_b128 v[220:223], v178 offset:22528
	ds_read_b128 v[224:227], v178 offset:23552
	global_load_lds_dwordx4 v[172:173], off
	s_add_i32 m0, s72, 0x2000
	s_add_u32 s72, s48, 0x80000
	v_lshl_add_u64 v[228:229], s[48:49], 0, v[136:137]
	s_addc_u32 s73, s49, 0
	s_add_i32 s74, s66, s52
	global_load_lds_dwordx4 v[228:229], off
	v_lshl_add_u64 v[230:231], s[72:73], 0, v[132:133]
	s_mov_b32 m0, s74
	v_lshl_add_u64 v[232:233], s[50:51], 0, v[134:135]
	global_load_lds_dwordx4 v[230:231], off
	v_lshl_add_u64 v[230:231], s[72:73], 0, v[136:137]
	s_add_i32 m0, s74, 0x2000
	s_nop 0
	global_load_lds_dwordx4 v[230:231], off
	v_lshl_add_u64 v[230:231], s[50:51], 0, v[130:131]
	s_mov_b32 m0, s53
	s_nop 0
	global_load_lds_dwordx4 v[230:231], off
	s_mov_b32 m0, s54
	s_nop 0
	global_load_lds_dwordx4 v[232:233], off
	s_waitcnt vmcnt(8)
	s_waitcnt lgkmcnt(0)
	s_setprio 1
	s_barrier
	v_mfma_f32_16x16x32_bf16 v[94:97], v[156:159], v[196:199], 0
	v_mfma_f32_16x16x32_bf16 v[90:93], v[164:167], v[196:199], 0
	v_mfma_f32_16x16x32_bf16 v[86:89], v[156:159], v[204:207], 0
	v_mfma_f32_16x16x32_bf16 v[82:85], v[164:167], v[204:207], 0
	v_mfma_f32_16x16x32_bf16 v[78:81], v[156:159], v[212:215], 0
	v_mfma_f32_16x16x32_bf16 v[74:77], v[164:167], v[212:215], 0
	v_mfma_f32_16x16x32_bf16 v[70:73], v[156:159], v[220:223], 0
	v_mfma_f32_16x16x32_bf16 v[66:69], v[164:167], v[220:223], 0
	v_mfma_f32_16x16x32_bf16 v[94:97], v[160:163], v[200:203], v[94:97]
	v_mfma_f32_16x16x32_bf16 v[90:93], v[168:171], v[200:203], v[90:93]
	v_mfma_f32_16x16x32_bf16 v[86:89], v[160:163], v[208:211], v[86:89]
	v_mfma_f32_16x16x32_bf16 v[82:85], v[168:171], v[208:211], v[82:85]
	v_mfma_f32_16x16x32_bf16 v[78:81], v[160:163], v[216:219], v[78:81]
	v_mfma_f32_16x16x32_bf16 v[74:77], v[168:171], v[216:219], v[74:77]
	v_mfma_f32_16x16x32_bf16 v[70:73], v[160:163], v[224:227], v[70:73]
	v_mfma_f32_16x16x32_bf16 v[66:69], v[168:171], v[224:227], v[66:69]
	s_setprio 0
	s_setprio 1
	v_mfma_f32_16x16x32_bf16 v[6:9], v[180:183], v[196:199], 0
	v_mfma_f32_16x16x32_bf16 v[2:5], v[188:191], v[196:199], 0
	v_mfma_f32_16x16x32_bf16 v[18:21], v[180:183], v[204:207], 0
	v_mfma_f32_16x16x32_bf16 v[14:17], v[188:191], v[204:207], 0
	v_mfma_f32_16x16x32_bf16 v[26:29], v[180:183], v[212:215], 0
	v_mfma_f32_16x16x32_bf16 v[22:25], v[188:191], v[212:215], 0
	v_mfma_f32_16x16x32_bf16 v[30:33], v[180:183], v[220:223], 0
	v_mfma_f32_16x16x32_bf16 v[10:13], v[188:191], v[220:223], 0
	v_mfma_f32_16x16x32_bf16 v[6:9], v[184:187], v[200:203], v[6:9]
	v_mfma_f32_16x16x32_bf16 v[2:5], v[192:195], v[200:203], v[2:5]
	v_mfma_f32_16x16x32_bf16 v[18:21], v[184:187], v[208:211], v[18:21]
	v_mfma_f32_16x16x32_bf16 v[14:17], v[192:195], v[208:211], v[14:17]
	v_mfma_f32_16x16x32_bf16 v[26:29], v[184:187], v[216:219], v[26:29]
	v_mfma_f32_16x16x32_bf16 v[22:25], v[192:195], v[216:219], v[22:25]
	v_mfma_f32_16x16x32_bf16 v[30:33], v[184:187], v[224:227], v[30:33]
	v_mfma_f32_16x16x32_bf16 v[10:13], v[192:195], v[224:227], v[10:13]
	s_barrier
	s_setprio 0
	s_add_i32 s72, 0, 0x18000
	v_add_u32_e32 v138, s72, v174
	s_add_i32 s73, 0, 0x1c000
	ds_read_b128 v[156:159], v138
	ds_read_b128 v[160:163], v138 offset:1024
	ds_read_b128 v[164:167], v138 offset:2048
	ds_read_b128 v[168:171], v138 offset:3072
	v_add_u32_e32 v138, s73, v174
	ds_read_b128 v[180:183], v138
	ds_read_b128 v[184:187], v138 offset:1024
	ds_read_b128 v[188:191], v138 offset:2048
	ds_read_b128 v[192:195], v138 offset:3072
	s_add_u32 s50, s50, 0x80000
	s_addc_u32 s51, s51, 0
	s_mov_b32 m0, s55
	v_lshl_add_u64 v[234:235], s[50:51], 0, v[130:131]
	ds_read_b128 v[196:199], v178 offset:32768
	ds_read_b128 v[200:203], v178 offset:33792
	ds_read_b128 v[204:207], v178 offset:34816
	ds_read_b128 v[208:211], v178 offset:35840
	ds_read_b128 v[212:215], v178 offset:36864
	ds_read_b128 v[216:219], v178 offset:37888
	ds_read_b128 v[220:223], v178 offset:38912
	ds_read_b128 v[224:227], v178 offset:39936
	global_load_lds_dwordx4 v[234:235], off
	v_lshl_add_u64 v[234:235], s[50:51], 0, v[134:135]
	s_mov_b32 m0, s56
	s_nop 0
	global_load_lds_dwordx4 v[234:235], off
	s_waitcnt vmcnt(8)
	s_waitcnt lgkmcnt(0)
	s_setprio 1
	s_barrier
	v_mfma_f32_16x16x32_bf16 v[126:129], v[156:159], v[196:199], v[126:129]
	v_mfma_f32_16x16x32_bf16 v[122:125], v[164:167], v[196:199], v[122:125]
	v_mfma_f32_16x16x32_bf16 v[118:121], v[156:159], v[204:207], v[118:121]
	v_mfma_f32_16x16x32_bf16 v[114:117], v[164:167], v[204:207], v[114:117]
	v_mfma_f32_16x16x32_bf16 v[110:113], v[156:159], v[212:215], v[110:113]
	v_mfma_f32_16x16x32_bf16 v[106:109], v[164:167], v[212:215], v[106:109]
	v_mfma_f32_16x16x32_bf16 v[102:105], v[156:159], v[220:223], v[102:105]
	v_mfma_f32_16x16x32_bf16 v[98:101], v[164:167], v[220:223], v[98:101]
	v_mfma_f32_16x16x32_bf16 v[126:129], v[160:163], v[200:203], v[126:129]
	v_mfma_f32_16x16x32_bf16 v[122:125], v[168:171], v[200:203], v[122:125]
	v_mfma_f32_16x16x32_bf16 v[118:121], v[160:163], v[208:211], v[118:121]
	v_mfma_f32_16x16x32_bf16 v[114:117], v[168:171], v[208:211], v[114:117]
	v_mfma_f32_16x16x32_bf16 v[110:113], v[160:163], v[216:219], v[110:113]
	v_mfma_f32_16x16x32_bf16 v[106:109], v[168:171], v[216:219], v[106:109]
	v_mfma_f32_16x16x32_bf16 v[102:105], v[160:163], v[224:227], v[102:105]
	v_mfma_f32_16x16x32_bf16 v[98:101], v[168:171], v[224:227], v[98:101]
	s_setprio 0
	s_setprio 1
	v_mfma_f32_16x16x32_bf16 v[38:41], v[180:183], v[196:199], v[38:41]
	v_mfma_f32_16x16x32_bf16 v[34:37], v[188:191], v[196:199], v[34:37]
	v_mfma_f32_16x16x32_bf16 v[46:49], v[180:183], v[204:207], v[46:49]
	v_mfma_f32_16x16x32_bf16 v[42:45], v[188:191], v[204:207], v[42:45]
	v_mfma_f32_16x16x32_bf16 v[54:57], v[180:183], v[212:215], v[54:57]
	v_mfma_f32_16x16x32_bf16 v[50:53], v[188:191], v[212:215], v[50:53]
	v_mfma_f32_16x16x32_bf16 v[62:65], v[180:183], v[220:223], v[62:65]
	v_mfma_f32_16x16x32_bf16 v[58:61], v[188:191], v[220:223], v[58:61]
	v_mfma_f32_16x16x32_bf16 v[38:41], v[184:187], v[200:203], v[38:41]
	v_mfma_f32_16x16x32_bf16 v[34:37], v[192:195], v[200:203], v[34:37]
	v_mfma_f32_16x16x32_bf16 v[46:49], v[184:187], v[208:211], v[46:49]
	v_mfma_f32_16x16x32_bf16 v[42:45], v[192:195], v[208:211], v[42:45]
	v_mfma_f32_16x16x32_bf16 v[54:57], v[184:187], v[216:219], v[54:57]
	v_mfma_f32_16x16x32_bf16 v[50:53], v[192:195], v[216:219], v[50:53]
	v_mfma_f32_16x16x32_bf16 v[62:65], v[184:187], v[224:227], v[62:65]
	v_mfma_f32_16x16x32_bf16 v[58:61], v[192:195], v[224:227], v[58:61]
	s_barrier
	s_setprio 0
	s_add_i32 s50, s72, s52
	v_lshl_add_u64 v[172:173], v[172:173], 0, s[6:7]
	s_mov_b32 m0, s50
	ds_read_b128 v[196:199], v178 offset:49152
	ds_read_b128 v[200:203], v178 offset:50176
	ds_read_b128 v[204:207], v178 offset:51200
	ds_read_b128 v[208:211], v178 offset:52224
	ds_read_b128 v[212:215], v178 offset:53248
	ds_read_b128 v[216:219], v178 offset:54272
	ds_read_b128 v[220:223], v178 offset:55296
	ds_read_b128 v[224:227], v178 offset:56320
	global_load_lds_dwordx4 v[172:173], off
	s_add_i32 m0, s50, 0x2000
	s_add_u32 s48, s48, 0x80080
	v_lshl_add_u64 v[172:173], v[228:229], 0, s[6:7]
	s_addc_u32 s49, s49, 0
	s_add_i32 s50, s73, s52
	global_load_lds_dwordx4 v[172:173], off
	v_lshl_add_u64 v[172:173], s[48:49], 0, v[132:133]
	s_mov_b32 m0, s50
	s_nop 0
	global_load_lds_dwordx4 v[172:173], off
	v_lshl_add_u64 v[172:173], s[48:49], 0, v[136:137]
	s_add_i32 m0, s50, 0x2000
	s_nop 0
	global_load_lds_dwordx4 v[172:173], off
	v_lshl_add_u64 v[172:173], v[230:231], 0, s[6:7]
	s_mov_b32 m0, s61
	s_nop 0
	global_load_lds_dwordx4 v[172:173], off
	v_lshl_add_u64 v[172:173], v[232:233], 0, s[6:7]
	s_mov_b32 m0, s62
	s_nop 0
	global_load_lds_dwordx4 v[172:173], off
	s_waitcnt vmcnt(8)
	s_waitcnt lgkmcnt(0)
	s_setprio 1
	s_barrier
	v_mfma_f32_16x16x32_bf16 v[94:97], v[156:159], v[196:199], v[94:97]
	v_mfma_f32_16x16x32_bf16 v[90:93], v[164:167], v[196:199], v[90:93]
	v_mfma_f32_16x16x32_bf16 v[86:89], v[156:159], v[204:207], v[86:89]
	v_mfma_f32_16x16x32_bf16 v[82:85], v[164:167], v[204:207], v[82:85]
	v_mfma_f32_16x16x32_bf16 v[78:81], v[156:159], v[212:215], v[78:81]
	v_mfma_f32_16x16x32_bf16 v[74:77], v[164:167], v[212:215], v[74:77]
	v_mfma_f32_16x16x32_bf16 v[70:73], v[156:159], v[220:223], v[70:73]
	v_mfma_f32_16x16x32_bf16 v[66:69], v[164:167], v[220:223], v[66:69]
	v_mfma_f32_16x16x32_bf16 v[94:97], v[160:163], v[200:203], v[94:97]
	v_mfma_f32_16x16x32_bf16 v[90:93], v[168:171], v[200:203], v[90:93]
	v_mfma_f32_16x16x32_bf16 v[86:89], v[160:163], v[208:211], v[86:89]
	v_mfma_f32_16x16x32_bf16 v[82:85], v[168:171], v[208:211], v[82:85]
	v_mfma_f32_16x16x32_bf16 v[78:81], v[160:163], v[216:219], v[78:81]
	v_mfma_f32_16x16x32_bf16 v[74:77], v[168:171], v[216:219], v[74:77]
	v_mfma_f32_16x16x32_bf16 v[70:73], v[160:163], v[224:227], v[70:73]
	v_mfma_f32_16x16x32_bf16 v[66:69], v[168:171], v[224:227], v[66:69]
	s_setprio 0
	s_setprio 1
	v_mfma_f32_16x16x32_bf16 v[6:9], v[180:183], v[196:199], v[6:9]
	v_mfma_f32_16x16x32_bf16 v[2:5], v[188:191], v[196:199], v[2:5]
	v_mfma_f32_16x16x32_bf16 v[18:21], v[180:183], v[204:207], v[18:21]
	v_mfma_f32_16x16x32_bf16 v[14:17], v[188:191], v[204:207], v[14:17]
	v_mfma_f32_16x16x32_bf16 v[26:29], v[180:183], v[212:215], v[26:29]
	v_mfma_f32_16x16x32_bf16 v[22:25], v[188:191], v[212:215], v[22:25]
	v_mfma_f32_16x16x32_bf16 v[30:33], v[180:183], v[220:223], v[30:33]
	v_mfma_f32_16x16x32_bf16 v[10:13], v[188:191], v[220:223], v[10:13]
	v_mfma_f32_16x16x32_bf16 v[6:9], v[184:187], v[200:203], v[6:9]
	v_mfma_f32_16x16x32_bf16 v[2:5], v[192:195], v[200:203], v[2:5]
	v_mfma_f32_16x16x32_bf16 v[18:21], v[184:187], v[208:211], v[18:21]
	v_mfma_f32_16x16x32_bf16 v[14:17], v[192:195], v[208:211], v[14:17]
	v_mfma_f32_16x16x32_bf16 v[26:29], v[184:187], v[216:219], v[26:29]
	v_mfma_f32_16x16x32_bf16 v[22:25], v[192:195], v[216:219], v[22:25]
	v_mfma_f32_16x16x32_bf16 v[30:33], v[184:187], v[224:227], v[30:33]
	v_mfma_f32_16x16x32_bf16 v[10:13], v[192:195], v[224:227], v[10:13]
	s_barrier
	s_setprio 0
	s_add_i32 s71, s71, 2
	s_add_u32 s46, s46, 0x100
	s_addc_u32 s47, s47, 0
	s_add_u32 s69, s69, 0x100
	s_addc_u32 s70, s70, 0
	s_cmp_gt_u32 s71, 29

.LBB0_2096:
	s_mov_b32 s101, 0
	s_mov_b32 s100, 0
	s_cmp_lt_i32 s78, 16
	s_cselect_b64 s[4:5], -1, 0
	s_and_b64 s[0:1], s[4:5], s[0:1]
	s_andn2_b64 vcc, exec, s[0:1]
	s_cbranch_vccnz .LBB0_2121
	v_readlane_b32 s4, v254, 14
	s_cmpk_gt_i32 s4, 0x3ff
	v_readfirstlane_b32 s12, v0
	s_cbranch_scc1 .LBB0_2121
	v_readlane_b32 s5, v254, 14
	s_ashr_i32 s33, s5, 31
	s_lshr_b32 s4, s33, 29
	s_add_i32 s7, s5, s4
	s_and_b32 s4, s7, -8
	s_sub_i32 s8, s5, s4
	s_cmp_gt_i32 s8, -1
	s_cbranch_scc0 .LBB0_2100
	s_lshl_b32 s6, s8, 7
	s_cbranch_execz .LBB0_2101
	s_branch .LBB0_2102

.LBB0_2113:
	s_ashr_i32 s25, s24, 31
	s_lshl_b64 s[26:27], s[24:25], 20
	v_readlane_b32 s28, v254, 22
	v_readlane_b32 s29, v254, 23
	s_add_u32 s26, s28, s26
	s_addc_u32 s27, s29, s27
	s_and_b64 s[28:29], s[4:5], exec
	s_cselect_b32 s25, s27, s35
	s_cselect_b32 s57, s26, s34
	s_ashr_i32 s23, s22, 31
	s_lshl_b64 s[28:29], s[22:23], 20
	s_add_u32 s28, s40, s28
	s_addc_u32 s29, s41, s29
	s_and_b64 s[38:39], s[4:5], exec
	s_cselect_b32 s23, s29, s37
	s_cselect_b32 s58, s28, s36
	s_add_u32 s34, s34, 0x80080
	s_addc_u32 s35, s35, 0
	s_add_u32 s59, s36, 0x100
	s_addc_u32 s60, s37, 0
	s_mov_b32 s61, -2
	s_cmp_lg_u32 s101, 0
	s_cbranch_scc0 .Lbs_2114
	s_barrier
	s_mov_b32 s101, 0
.Lbs_2114:
	ds_read_b128 v[154:157], v150
	ds_read_b128 v[158:161], v150 offset:1024
	ds_read_b128 v[162:165], v150 offset:2048
	ds_read_b128 v[166:169], v150 offset:3072
	ds_read_b128 v[170:173], v151
	ds_read_b128 v[174:177], v151 offset:1024
	ds_read_b128 v[178:181], v151 offset:2048
	ds_read_b128 v[182:185], v151 offset:3072
	s_add_u32 s36, s34, 0xfff80080
	s_addc_u32 s37, s35, -1
	s_cmp_eq_u32 s61, 28
	s_cselect_b32 s39, s25, s37
	s_cselect_b32 s38, s57, s36
	s_cselect_b32 s37, s23, s60
	s_cselect_b32 s36, s58, s59
	v_lshl_add_u64 v[146:147], s[34:35], 0, v[138:139]
	s_add_i32 m0, s31, 0xc000
	ds_read_b128 v[186:189], v152
	ds_read_b128 v[190:193], v152 offset:1024
	ds_read_b128 v[194:197], v152 offset:2048
	ds_read_b128 v[198:201], v152 offset:3072
	ds_read_b128 v[202:205], v152 offset:4096
	ds_read_b128 v[206:209], v152 offset:5120
	ds_read_b128 v[210:213], v152 offset:6144
	ds_read_b128 v[214:217], v152 offset:7168
	global_load_lds_dwordx4 v[146:147], off
	v_lshl_add_u64 v[146:147], s[34:35], 0, v[140:141]
	s_add_i32 m0, s31, 0xe000
	s_nop 0
	global_load_lds_dwordx4 v[146:147], off
	s_cmp_lg_u32 s100, 0
	s_cbranch_scc1 .Lrx_2114_0
	s_waitcnt vmcnt(8)

.LBB0_2117:
	v_lshl_add_u32 v154, s30, 8, v1
	v_lshl_or_b32 v146, s56, 8, v149
	v_ashrrev_i32_e32 v155, 31, v154
	v_ashrrev_i32_e32 v147, 31, v146
	v_lshlrev_b64 v[156:157], 12, v[154:155]
	v_lshl_add_u64 v[156:157], s[2:3], 0, v[156:157]
	v_lshlrev_b64 v[158:159], 1, v[146:147]
	v_lshl_add_u64 v[146:147], v[156:157], 0, v[158:159]
	v_cvt_pk_bf16_f32 v126, v126, v127
	v_cvt_pk_bf16_f32 v127, v128, v129
	v_cvt_pk_bf16_f32 v128, v122, v123
	v_cvt_pk_bf16_f32 v129, v124, v125
	global_store_dwordx4 v[146:147], v[126:129], off
	v_cvt_pk_bf16_f32 v114, v114, v115
	v_cvt_pk_bf16_f32 v115, v116, v117
	v_cvt_pk_bf16_f32 v116, v106, v107
	v_or_b32_e32 v106, 16, v154
	v_ashrrev_i32_e32 v107, 31, v106
	v_lshlrev_b64 v[106:107], 12, v[106:107]
	v_lshl_add_u64 v[106:107], s[2:3], 0, v[106:107]
	v_cvt_pk_bf16_f32 v117, v108, v109
	global_store_dwordx4 v[146:147], v[114:117], off offset:256
	s_nop 1
	v_lshl_add_u64 v[114:115], v[106:107], 0, v[158:159]
	v_cvt_pk_bf16_f32 v106, v118, v119
	v_cvt_pk_bf16_f32 v107, v120, v121
	v_cvt_pk_bf16_f32 v108, v110, v111
	v_cvt_pk_bf16_f32 v109, v112, v113
	global_store_dwordx4 v[114:115], v[106:109], off
	v_cvt_pk_bf16_f32 v98, v98, v99
	v_cvt_pk_bf16_f32 v99, v100, v101
	v_cvt_pk_bf16_f32 v100, v90, v91
	v_or_b32_e32 v90, 32, v154
	v_ashrrev_i32_e32 v91, 31, v90
	v_lshlrev_b64 v[90:91], 12, v[90:91]
	v_lshl_add_u64 v[90:91], s[2:3], 0, v[90:91]
	v_cvt_pk_bf16_f32 v101, v92, v93
	global_store_dwordx4 v[114:115], v[98:101], off offset:256
	s_nop 1
	v_lshl_add_u64 v[98:99], v[90:91], 0, v[158:159]
	v_cvt_pk_bf16_f32 v90, v102, v103
	v_cvt_pk_bf16_f32 v91, v104, v105
	v_cvt_pk_bf16_f32 v92, v94, v95
	v_cvt_pk_bf16_f32 v93, v96, v97
	global_store_dwordx4 v[98:99], v[90:93], off
	v_cvt_pk_bf16_f32 v82, v82, v83
	v_cvt_pk_bf16_f32 v83, v84, v85
	v_cvt_pk_bf16_f32 v84, v74, v75
	v_or_b32_e32 v74, 48, v154
	v_ashrrev_i32_e32 v75, 31, v74
	v_lshlrev_b64 v[74:75], 12, v[74:75]
	v_lshl_add_u64 v[74:75], s[2:3], 0, v[74:75]
	v_cvt_pk_bf16_f32 v85, v76, v77
	global_store_dwordx4 v[98:99], v[82:85], off offset:256
	s_nop 1
	v_lshl_add_u64 v[82:83], v[74:75], 0, v[158:159]
	v_cvt_pk_bf16_f32 v74, v86, v87
	v_cvt_pk_bf16_f32 v75, v88, v89
	v_cvt_pk_bf16_f32 v76, v78, v79
	v_cvt_pk_bf16_f32 v77, v80, v81
	global_store_dwordx4 v[82:83], v[74:77], off
	v_cvt_pk_bf16_f32 v70, v70, v71
	v_cvt_pk_bf16_f32 v71, v72, v73
	v_cvt_pk_bf16_f32 v72, v66, v67
	v_cvt_pk_bf16_f32 v73, v68, v69
	global_store_dwordx4 v[82:83], v[70:73], off offset:256
	v_cvt_pk_bf16_f32 v62, v62, v63
	v_cvt_pk_bf16_f32 v63, v64, v65
	v_cvt_pk_bf16_f32 v64, v58, v59
	v_add_co_u32_e32 v58, vcc, s52, v146
	v_lshl_add_u64 v[66:67], v[146:147], 0, s[6:7]
	s_nop 0
	v_addc_co_u32_e32 v59, vcc, 0, v147, vcc
	v_cvt_pk_bf16_f32 v65, v60, v61
	global_store_dwordx4 v[58:59], v[62:65], off
	v_cvt_pk_bf16_f32 v50, v50, v51
	v_cvt_pk_bf16_f32 v51, v52, v53
	v_cvt_pk_bf16_f32 v52, v42, v43
	v_cvt_pk_bf16_f32 v53, v44, v45
	global_store_dwordx4 v[66:67], v[50:53], off offset:256
	v_cvt_pk_bf16_f32 v42, v54, v55
	v_cvt_pk_bf16_f32 v43, v56, v57
	v_cvt_pk_bf16_f32 v44, v46, v47
	v_add_co_u32_e32 v46, vcc, s53, v146
	s_nop 0
	v_lshl_add_u64 v[50:51], v[146:147], 0, s[14:15]
	v_addc_co_u32_e32 v47, vcc, 0, v147, vcc
	v_cvt_pk_bf16_f32 v45, v48, v49
	global_store_dwordx4 v[46:47], v[42:45], off
	v_cvt_pk_bf16_f32 v34, v34, v35
	v_cvt_pk_bf16_f32 v35, v36, v37
	v_cvt_pk_bf16_f32 v36, v26, v27
	v_cvt_pk_bf16_f32 v37, v28, v29
	global_store_dwordx4 v[50:51], v[34:37], off offset:256
	v_cvt_pk_bf16_f32 v26, v38, v39
	v_cvt_pk_bf16_f32 v27, v40, v41
	v_cvt_pk_bf16_f32 v28, v30, v31
	v_add_co_u32_e32 v30, vcc, s54, v146
	s_nop 0
	v_lshl_add_u64 v[34:35], v[146:147], 0, s[16:17]
	v_addc_co_u32_e32 v31, vcc, 0, v147, vcc
	v_cvt_pk_bf16_f32 v29, v32, v33
	global_store_dwordx4 v[30:31], v[26:29], off
	v_cvt_pk_bf16_f32 v18, v18, v19
	v_cvt_pk_bf16_f32 v19, v20, v21
	v_cvt_pk_bf16_f32 v20, v10, v11
	v_cvt_pk_bf16_f32 v21, v12, v13
	global_store_dwordx4 v[34:35], v[18:21], off offset:256
	v_cvt_pk_bf16_f32 v10, v22, v23
	v_cvt_pk_bf16_f32 v11, v24, v25
	v_cvt_pk_bf16_f32 v12, v14, v15
	v_add_co_u32_e32 v14, vcc, s55, v146
	s_nop 0
	v_lshl_add_u64 v[18:19], v[146:147], 0, s[18:19]
	v_addc_co_u32_e32 v15, vcc, 0, v147, vcc
	s_andn2_b64 vcc, exec, s[4:5]
	s_mov_b64 s[4:5], -1
	v_cvt_pk_bf16_f32 v13, v16, v17
	global_store_dwordx4 v[14:15], v[10:13], off
	v_cvt_pk_bf16_f32 v6, v6, v7
	v_cvt_pk_bf16_f32 v7, v8, v9
	v_cvt_pk_bf16_f32 v8, v2, v3
	v_cvt_pk_bf16_f32 v9, v4, v5
	global_store_dwordx4 v[18:19], v[6:9], off offset:256
	s_cbranch_vccnz .LBB0_2106
	s_andn2_b64 vcc, exec, s[8:9]
	s_cbranch_vccnz .LBB0_2105
	s_mov_b32 s101, 1
	s_branch .LBB0_2105

.LBB0_2356:
	s_mov_b32 s101, 0
	s_mov_b32 s100, 0
	s_cmp_lt_i32 s78, 19
	s_cselect_b64 s[2:3], -1, 0
	s_min_u32 s58, s50, 0x108
	s_and_b64 s[2:3], s[2:3], s[0:1]
	s_cmp_gt_i32 s50, 0
	s_cselect_b64 s[0:1], -1, 0
	s_and_b64 s[4:5], s[2:3], s[0:1]
	s_andn2_b64 vcc, exec, s[4:5]
	s_mov_b32 s74, s66
	s_cbranch_vccnz .LBB0_2373
	s_mul_i32 s6, s58, 56
	v_readlane_b32 s4, v254, 14
	s_cmp_ge_i32 s4, s6
	v_readfirstlane_b32 s4, v0
	s_cbranch_scc1 .LBB0_2373
	v_lshrrev_b32_e32 v1, 5, v0
	v_lshrrev_b32_e32 v3, 1, v0
	v_and_b32_e32 v1, 4, v1
	v_bfe_u32 v2, v0, 2, 2
	s_waitcnt lgkmcnt(0)
	v_and_b32_e32 v13, 24, v3
	s_add_u32 s19, s86, 0x25800000
	v_or3_b32 v1, v1, v2, v13
	v_lshlrev_b32_e32 v2, 4, v0
	s_addc_u32 s40, s87, 0
	v_or_b32_e32 v10, 0x2000, v2
	s_add_u32 s41, s86, 0x8800000
	v_lshrrev_b32_e32 v3, 7, v10
	s_movk_i32 s7, 0x60
	v_readlane_b32 s9, v254, 14
	s_addc_u32 s42, s87, 0
	v_and_or_b32 v4, v3, s7, v1
	v_bfe_u32 v14, v0, 2, 4
	s_movk_i32 s7, 0x70
	s_ashr_i32 s45, s9, 31
	v_and_or_b32 v3, v3, s7, v14
	s_lshr_b32 s7, s45, 29
	s_add_i32 s7, s9, s7
	s_lshr_b32 s12, s4, 6
	s_mul_i32 s44, s58, 7
	s_ashr_i32 s8, s7, 3
	s_and_b32 s7, s7, -8
	s_lshr_b32 s5, s4, 8
	s_lshl_b32 s43, s12, 10
	s_sub_i32 s7, s9, s7
	s_add_i32 s46, s44, 1
	s_cmp_lt_i32 s7, 0
	s_cselect_b32 s9, s46, s44
	s_mul_i32 s7, s9, s7
	s_add_i32 s7, s7, s8
	s_mul_hi_i32 s8, s7, 0x92492493
	s_add_i32 s8, s8, s7
	s_lshr_b32 s9, s8, 31
	s_ashr_i32 s8, s8, 8
	s_add_i32 s8, s8, s9
	s_lshl_b32 s9, s8, 3
	v_and_b32_e32 v5, 32, v0
	s_sub_i32 s10, s58, s9
	v_bitop3_b32 v11, v2, v5, 48 bitop3:0x6c
	v_and_b32_e32 v12, 64, v0
	s_min_i32 s10, s10, 8
	v_or_b32_e32 v2, v11, v12
	s_abs_i32 s11, s10
	s_waitcnt vmcnt(0)
	v_lshl_or_b32 v162, v4, 11, v2
	v_cvt_f32_u32_e32 v4, s11
	v_lshl_or_b32 v164, v3, 11, v2
	v_lshrrev_b32_e32 v3, 3, v0
	v_and_or_b32 v1, v3, 32, v1
	v_lshl_or_b32 v166, v1, 11, v2
	v_and_or_b32 v1, v3, 48, v14
	v_lshl_or_b32 v168, v1, 11, v2
	v_rcp_iflag_f32_e32 v1, v4
	s_sub_i32 s16, 0, s11
	s_mulk_i32 s8, 0x1c0
	s_sub_i32 s7, s7, s8
	v_mul_f32_e32 v1, 0x4f7ffffe, v1
	v_cvt_u32_f32_e32 v1, v1
	s_abs_i32 s13, s7
	s_xor_b32 s8, s7, s10
	s_ashr_i32 s8, s8, 31
	v_readfirstlane_b32 s17, v1
	s_mul_i32 s16, s16, s17
	s_mul_hi_u32 s16, s17, s16
	s_add_i32 s17, s17, s16
	s_mul_hi_u32 s16, s13, s17
	s_mul_i32 s17, s16, s11
	s_sub_i32 s13, s13, s17
	s_add_i32 s17, s16, 1
	s_sub_i32 s18, s13, s11
	s_cmp_ge_u32 s13, s11
	s_cselect_b32 s16, s17, s16
	s_cselect_b32 s13, s18, s13
	s_add_i32 s17, s16, 1
	s_cmp_ge_u32 s13, s11
	s_cselect_b32 s11, s17, s16
	s_xor_b32 s11, s11, s8
	s_sub_i32 s65, s11, s8
	s_mul_i32 s8, s65, s10
	s_sub_i32 s7, s7, s8
	s_add_i32 s30, s9, s7
	s_cmp_ge_i32 s30, s33
	s_cselect_b64 s[8:9], -1, 0
	s_cmp_ge_i32 s30, s57
	v_cndmask_b32_e64 v1, 0, 1, s[8:9]
	s_cselect_b64 s[8:9], -1, 0
	s_cmp_ge_i32 s30, s52
	v_cndmask_b32_e64 v2, 0, 1, s[8:9]
	s_cselect_b64 s[8:9], -1, 0
	v_readfirstlane_b32 s7, v1
	v_readfirstlane_b32 s10, v2
	s_cmp_lg_u64 s[8:9], 0
	s_addc_u32 s7, s7, s10
	s_cmp_ge_i32 s30, s53
	s_cselect_b64 s[8:9], -1, 0
	s_cmp_ge_i32 s30, s54
	v_cndmask_b32_e64 v1, 0, 1, s[8:9]
	s_cselect_b64 s[8:9], -1, 0
	v_readfirstlane_b32 s10, v1
	s_cmp_lg_u64 s[8:9], 0
	s_addc_u32 s7, s7, s10
	s_cmp_ge_i32 s30, s55
	s_cselect_b64 s[8:9], -1, 0
	s_cmp_ge_i32 s30, s56
	v_cndmask_b32_e64 v1, 0, 1, s[8:9]
	s_cselect_b64 s[8:9], -1, 0
	v_readfirstlane_b32 s10, v1
	s_cmp_lg_u64 s[8:9], 0
	s_addc_u32 s7, s7, s10
	s_mul_i32 s7, s7, 56
	s_add_i32 s8, s7, s65
	s_ashr_i32 s9, s8, 31
	s_ashr_i32 s31, s30, 31
	s_lshl_b64 s[8:9], s[8:9], 19
	s_lshl_b64 s[10:11], s[30:31], 19
	s_add_u32 s36, s41, s8
	s_addc_u32 s37, s42, s9
	s_add_i32 s31, s43, 0
	s_add_i32 m0, s31, 0x10000
	v_mov_b32_e32 v167, 0
	global_load_lds_dwordx4 v166, s[36:37]
	s_add_i32 m0, s31, 0x12000
	s_add_u32 s8, s36, 0x40000
	global_load_lds_dwordx4 v162, s[36:37]
	s_addc_u32 s9, s37, 0
	s_add_i32 m0, s31, 0x14000
	v_mov_b32_e32 v163, v167
	global_load_lds_dwordx4 v166, s[8:9]
	s_add_i32 m0, s31, 0x16000
	s_add_u32 s34, s19, s10
	s_addc_u32 s35, s40, s11
	s_add_i32 s47, s31, 0x2000
	global_load_lds_dwordx4 v162, s[8:9]
	s_mov_b32 m0, s31
	s_add_u32 s8, s34, 0x40000
	global_load_lds_dwordx4 v168, s[34:35]
	s_mov_b32 m0, s47
	s_addc_u32 s9, s35, 0
	s_add_i32 s48, s31, 0x4000
	global_load_lds_dwordx4 v164, s[34:35]
	s_mov_b32 m0, s48
	s_add_i32 s49, s31, 0x6000
	global_load_lds_dwordx4 v168, s[8:9]
	s_mov_b32 m0, s49
	v_mov_b32_e32 v169, v167
	global_load_lds_dwordx4 v164, s[8:9]
	v_mov_b32_e32 v165, v167
	s_cmp_eq_u32 s5, 1
	s_mov_b32 s7, 0
	v_lshl_add_u64 v[8:9], s[36:37], 0, v[166:167]
	v_lshl_add_u64 v[6:7], s[36:37], 0, v[162:163]
	v_lshl_add_u64 v[2:3], s[34:35], 0, v[168:169]
	s_cselect_b64 s[8:9], -1, 0
	s_cmp_lg_u32 s5, 1
	v_lshl_add_u64 v[4:5], s[34:35], 0, v[164:165]
	s_cbranch_scc1 .LBB0_2360
	s_barrier

.LBB0_2365:
	s_ashr_i32 s23, s22, 31
	s_lshl_b64 s[26:27], s[22:23], 19
	s_add_u32 s26, s19, s26
	s_addc_u32 s27, s40, s27
	s_and_b64 s[28:29], s[4:5], exec
	s_cselect_b32 s23, s27, s35
	s_cselect_b32 s66, s26, s34
	s_ashr_i32 s25, s24, 31
	s_lshl_b64 s[28:29], s[24:25], 19
	s_add_u32 s28, s41, s28
	s_addc_u32 s29, s42, s29
	s_and_b64 s[38:39], s[4:5], exec
	s_cselect_b32 s25, s29, s37
	s_cselect_b32 s67, s28, s36
	s_add_u32 s34, s34, 0x40080
	s_addc_u32 s35, s35, 0
	s_add_u32 s68, s36, 0x100
	s_addc_u32 s69, s37, 0
	s_mov_b32 s70, -2
	s_cmp_lg_u32 s101, 0
	s_cbranch_scc0 .Lbs_2366
	s_barrier
	s_mov_b32 s101, 0
.Lbs_2366:
	ds_read_b128 v[18:21], v186
	ds_read_b128 v[22:25], v186 offset:1024
	ds_read_b128 v[26:29], v186 offset:2048
	ds_read_b128 v[30:33], v186 offset:3072
	ds_read_b128 v[2:5], v187
	ds_read_b128 v[6:9], v187 offset:1024
	ds_read_b128 v[10:13], v187 offset:2048
	ds_read_b128 v[14:17], v187 offset:3072
	s_add_u32 s36, s34, 0xfffc0080
	s_addc_u32 s37, s35, -1
	s_cmp_eq_u32 s70, 12
	s_cselect_b32 s39, s23, s37
	s_cselect_b32 s38, s66, s36
	s_cselect_b32 s37, s25, s69
	s_cselect_b32 s36, s67, s68
	v_lshl_add_u64 v[208:209], s[34:35], 0, v[170:171]
	s_add_i32 m0, s31, 0xc000
	ds_read_b128 v[176:179], v188
	ds_read_b128 v[180:183], v188 offset:1024
	ds_read_b128 v[192:195], v188 offset:2048
	ds_read_b128 v[196:199], v188 offset:3072
	ds_read_b128 v[200:203], v188 offset:4096
	ds_read_b128 v[204:207], v188 offset:5120
	ds_read_b128 v[216:219], v188 offset:6144
	ds_read_b128 v[220:223], v188 offset:7168
	global_load_lds_dwordx4 v[208:209], off
	v_lshl_add_u64 v[208:209], s[34:35], 0, v[172:173]
	s_add_i32 m0, s31, 0xe000
	s_nop 0
	global_load_lds_dwordx4 v[208:209], off
	s_cmp_lg_u32 s100, 0
	s_cbranch_scc1 .Lrx_2366_0
	s_waitcnt vmcnt(8)

.LBB0_2369:
	v_pk_mul_f32 v[8:9], v[160:161], s[6:7] op_sel_hi:[1,0]
	v_pk_mul_f32 v[4:5], v[158:159], s[6:7] op_sel_hi:[1,0]
	v_exp_f32_e32 v8, v8
	v_exp_f32_e32 v9, v9
	v_exp_f32_e32 v4, v4
	v_exp_f32_e32 v5, v5
	v_pk_mul_f32 v[10:11], v[160:161], v[156:157]
	v_pk_fma_f32 v[8:9], v[8:9], s[18:19], s[18:19] op_sel_hi:[1,0,0]
	v_pk_mul_f32 v[12:13], v[158:159], v[154:155]
	v_pk_fma_f32 v[4:5], v[4:5], s[18:19], s[18:19] op_sel_hi:[1,0,0]
	v_rcp_f32_e32 v8, v8
	v_rcp_f32_e32 v9, v9
	v_rcp_f32_e32 v4, v4
	v_rcp_f32_e32 v5, v5
	v_pk_mul_f32 v[16:17], v[150:151], v[146:147]
	v_pk_mul_f32 v[8:9], v[10:11], v[8:9]
	v_pk_mul_f32 v[10:11], v[150:151], s[6:7] op_sel_hi:[1,0]
	v_pk_mul_f32 v[4:5], v[12:13], v[4:5]
	v_exp_f32_e32 v10, v10
	v_exp_f32_e32 v11, v11
	v_pk_mul_f32 v[12:13], v[152:153], s[6:7] op_sel_hi:[1,0]
	v_pk_mul_f32 v[14:15], v[152:153], v[148:149]
	v_exp_f32_e32 v12, v12
	v_exp_f32_e32 v13, v13
	v_pk_fma_f32 v[10:11], v[10:11], s[18:19], s[18:19] op_sel_hi:[1,0,0]
	v_med3_f32 v4, v4, s62, v191
	v_rcp_f32_e32 v10, v10
	v_rcp_f32_e32 v11, v11
	v_pk_fma_f32 v[12:13], v[12:13], s[18:19], s[18:19] op_sel_hi:[1,0,0]
	v_med3_f32 v5, v5, s62, v191
	v_rcp_f32_e32 v12, v12
	v_rcp_f32_e32 v13, v13
	v_pk_mul_f32 v[10:11], v[16:17], v[10:11]
	v_med3_f32 v7, v8, s62, v191
	v_mov_b32_e32 v8, 0
	v_pk_mul_f32 v[12:13], v[14:15], v[12:13]
	v_med3_f32 v14, v9, s62, v191
	v_cvt_pk_fp8_f32 v8, v4, v5
	v_med3_f32 v4, v10, s62, v191
	v_med3_f32 v5, v11, s62, v191
	v_mov_b32_e32 v9, 0
	v_cvt_pk_fp8_f32 v9, v4, v5
	v_med3_f32 v4, v12, s62, v191
	v_med3_f32 v5, v13, s62, v191
	v_cvt_pk_fp8_f32 v8, v7, v14 op_sel:[0,0,1]
	v_cvt_pk_fp8_f32 v9, v4, v5 op_sel:[0,0,1]
	v_lshl_add_u32 v6, s30, 8, v1
	v_lshl_or_b32 v2, s65, 7, v185
	v_mov_b64_e32 v[4:5], s[10:11]
	v_ashrrev_i32_e32 v3, 31, v2
	v_mad_i64_i32 v[10:11], s[34:35], v6, s63, v[4:5]
	v_lshl_add_u64 v[10:11], v[10:11], 0, v[2:3]
	s_nop 15
	s_nop 15
	global_store_dwordx2 v[10:11], v[8:9], off
	v_pk_mul_f32 v[10:11], v[144:145], s[6:7] op_sel_hi:[1,0]
	v_pk_mul_f32 v[8:9], v[142:143], s[6:7] op_sel_hi:[1,0]
	v_exp_f32_e32 v10, v10
	v_exp_f32_e32 v11, v11
	v_exp_f32_e32 v8, v8
	v_exp_f32_e32 v9, v9
	v_pk_mul_f32 v[12:13], v[144:145], v[140:141]
	v_pk_fma_f32 v[10:11], v[10:11], s[18:19], s[18:19] op_sel_hi:[1,0,0]
	v_pk_mul_f32 v[14:15], v[142:143], v[138:139]
	v_rcp_f32_e32 v10, v10
	v_rcp_f32_e32 v11, v11
	v_pk_fma_f32 v[8:9], v[8:9], s[18:19], s[18:19] op_sel_hi:[1,0,0]
	v_pk_mul_f32 v[18:19], v[134:135], v[130:131]
	v_rcp_f32_e32 v8, v8
	v_rcp_f32_e32 v9, v9
	v_pk_mul_f32 v[10:11], v[12:13], v[10:11]
	v_pk_mul_f32 v[12:13], v[134:135], s[6:7] op_sel_hi:[1,0]
	v_pk_mul_f32 v[16:17], v[136:137], v[132:133]
	v_exp_f32_e32 v12, v12
	v_exp_f32_e32 v13, v13
	v_pk_mul_f32 v[8:9], v[14:15], v[8:9]
	v_pk_mul_f32 v[14:15], v[136:137], s[6:7] op_sel_hi:[1,0]
	v_med3_f32 v7, v8, s62, v191
	v_exp_f32_e32 v14, v14
	v_exp_f32_e32 v15, v15
	v_pk_fma_f32 v[12:13], v[12:13], s[18:19], s[18:19] op_sel_hi:[1,0,0]
	v_med3_f32 v9, v9, s62, v191
	v_rcp_f32_e32 v12, v12
	v_rcp_f32_e32 v13, v13
	v_pk_fma_f32 v[14:15], v[14:15], s[18:19], s[18:19] op_sel_hi:[1,0,0]
	v_mov_b32_e32 v8, 0
	v_rcp_f32_e32 v14, v14
	v_rcp_f32_e32 v15, v15
	v_pk_mul_f32 v[12:13], v[18:19], v[12:13]
	v_cvt_pk_fp8_f32 v8, v7, v9
	v_med3_f32 v7, v12, s62, v191
	v_med3_f32 v12, v13, s62, v191
	v_mov_b32_e32 v9, 0
	v_cvt_pk_fp8_f32 v9, v7, v12
	v_pk_mul_f32 v[14:15], v[16:17], v[14:15]
	v_med3_f32 v10, v10, s62, v191
	v_med3_f32 v11, v11, s62, v191
	v_cvt_pk_fp8_f32 v8, v10, v11 op_sel:[0,0,1]
	v_med3_f32 v7, v14, s62, v191
	v_med3_f32 v10, v15, s62, v191
	v_cvt_pk_fp8_f32 v9, v7, v10 op_sel:[0,0,1]
	v_or_b32_e32 v7, 16, v6
	v_mad_i64_i32 v[10:11], s[34:35], v7, s63, v[4:5]
	v_lshl_add_u64 v[10:11], v[10:11], 0, v[2:3]
	global_store_dwordx2 v[10:11], v[8:9], off
	v_pk_mul_f32 v[10:11], v[128:129], s[6:7] op_sel_hi:[1,0]
	v_pk_mul_f32 v[8:9], v[126:127], s[6:7] op_sel_hi:[1,0]
	v_exp_f32_e32 v10, v10
	v_exp_f32_e32 v11, v11
	v_exp_f32_e32 v8, v8
	v_exp_f32_e32 v9, v9
	v_pk_mul_f32 v[12:13], v[128:129], v[124:125]
	v_pk_fma_f32 v[10:11], v[10:11], s[18:19], s[18:19] op_sel_hi:[1,0,0]
	v_pk_mul_f32 v[14:15], v[126:127], v[122:123]
	v_rcp_f32_e32 v10, v10
	v_rcp_f32_e32 v11, v11
	v_pk_fma_f32 v[8:9], v[8:9], s[18:19], s[18:19] op_sel_hi:[1,0,0]
	v_pk_mul_f32 v[18:19], v[118:119], v[114:115]
	v_rcp_f32_e32 v8, v8
	v_rcp_f32_e32 v9, v9
	v_pk_mul_f32 v[10:11], v[12:13], v[10:11]
	v_pk_mul_f32 v[12:13], v[118:119], s[6:7] op_sel_hi:[1,0]
	v_pk_mul_f32 v[16:17], v[120:121], v[116:117]
	v_exp_f32_e32 v12, v12
	v_exp_f32_e32 v13, v13
	v_pk_mul_f32 v[8:9], v[14:15], v[8:9]
	v_pk_mul_f32 v[14:15], v[120:121], s[6:7] op_sel_hi:[1,0]
	v_med3_f32 v7, v8, s62, v191
	v_exp_f32_e32 v14, v14
	v_exp_f32_e32 v15, v15
	v_pk_fma_f32 v[12:13], v[12:13], s[18:19], s[18:19] op_sel_hi:[1,0,0]
	v_med3_f32 v9, v9, s62, v191
	v_rcp_f32_e32 v12, v12
	v_rcp_f32_e32 v13, v13
	v_pk_fma_f32 v[14:15], v[14:15], s[18:19], s[18:19] op_sel_hi:[1,0,0]
	v_mov_b32_e32 v8, 0
	v_rcp_f32_e32 v14, v14
	v_rcp_f32_e32 v15, v15
	v_pk_mul_f32 v[12:13], v[18:19], v[12:13]
	v_cvt_pk_fp8_f32 v8, v7, v9
	v_med3_f32 v7, v12, s62, v191
	v_med3_f32 v12, v13, s62, v191
	v_mov_b32_e32 v9, 0
	v_cvt_pk_fp8_f32 v9, v7, v12
	v_pk_mul_f32 v[14:15], v[16:17], v[14:15]
	v_med3_f32 v10, v10, s62, v191
	v_med3_f32 v11, v11, s62, v191
	v_cvt_pk_fp8_f32 v8, v10, v11 op_sel:[0,0,1]
	v_med3_f32 v7, v14, s62, v191
	v_med3_f32 v10, v15, s62, v191
	v_cvt_pk_fp8_f32 v9, v7, v10 op_sel:[0,0,1]
	v_or_b32_e32 v7, 32, v6
	v_mad_i64_i32 v[10:11], s[34:35], v7, s63, v[4:5]
	v_lshl_add_u64 v[10:11], v[10:11], 0, v[2:3]
	global_store_dwordx2 v[10:11], v[8:9], off
	v_pk_mul_f32 v[10:11], v[112:113], s[6:7] op_sel_hi:[1,0]
	v_pk_mul_f32 v[8:9], v[110:111], s[6:7] op_sel_hi:[1,0]
	v_exp_f32_e32 v10, v10
	v_exp_f32_e32 v11, v11
	v_exp_f32_e32 v8, v8
	v_exp_f32_e32 v9, v9
	v_pk_mul_f32 v[12:13], v[112:113], v[108:109]
	v_pk_fma_f32 v[10:11], v[10:11], s[18:19], s[18:19] op_sel_hi:[1,0,0]
	v_pk_mul_f32 v[14:15], v[110:111], v[106:107]
	v_rcp_f32_e32 v10, v10
	v_rcp_f32_e32 v11, v11
	v_pk_fma_f32 v[8:9], v[8:9], s[18:19], s[18:19] op_sel_hi:[1,0,0]
	v_pk_mul_f32 v[18:19], v[102:103], v[98:99]
	v_rcp_f32_e32 v8, v8
	v_rcp_f32_e32 v9, v9
	v_pk_mul_f32 v[10:11], v[12:13], v[10:11]
	v_pk_mul_f32 v[12:13], v[102:103], s[6:7] op_sel_hi:[1,0]
	v_pk_mul_f32 v[16:17], v[104:105], v[100:101]
	v_exp_f32_e32 v12, v12
	v_exp_f32_e32 v13, v13
	v_pk_mul_f32 v[8:9], v[14:15], v[8:9]
	v_pk_mul_f32 v[14:15], v[104:105], s[6:7] op_sel_hi:[1,0]
	v_med3_f32 v7, v8, s62, v191
	v_exp_f32_e32 v14, v14
	v_exp_f32_e32 v15, v15
	v_pk_fma_f32 v[12:13], v[12:13], s[18:19], s[18:19] op_sel_hi:[1,0,0]
	v_med3_f32 v9, v9, s62, v191
	v_rcp_f32_e32 v12, v12
	v_rcp_f32_e32 v13, v13
	v_pk_fma_f32 v[14:15], v[14:15], s[18:19], s[18:19] op_sel_hi:[1,0,0]
	v_mov_b32_e32 v8, 0
	v_rcp_f32_e32 v14, v14
	v_rcp_f32_e32 v15, v15
	v_pk_mul_f32 v[12:13], v[18:19], v[12:13]
	v_cvt_pk_fp8_f32 v8, v7, v9
	v_med3_f32 v7, v12, s62, v191
	v_med3_f32 v12, v13, s62, v191
	v_mov_b32_e32 v9, 0
	v_cvt_pk_fp8_f32 v9, v7, v12
	v_pk_mul_f32 v[14:15], v[16:17], v[14:15]
	v_med3_f32 v10, v10, s62, v191
	v_med3_f32 v11, v11, s62, v191
	v_cvt_pk_fp8_f32 v8, v10, v11 op_sel:[0,0,1]
	v_med3_f32 v7, v14, s62, v191
	v_med3_f32 v10, v15, s62, v191
	v_cvt_pk_fp8_f32 v9, v7, v10 op_sel:[0,0,1]
	v_or_b32_e32 v7, 48, v6
	v_mad_i64_i32 v[10:11], s[34:35], v7, s63, v[4:5]
	v_lshl_add_u64 v[10:11], v[10:11], 0, v[2:3]
	global_store_dwordx2 v[10:11], v[8:9], off
	v_pk_mul_f32 v[8:9], v[94:95], s[6:7] op_sel_hi:[1,0]
	v_pk_mul_f32 v[10:11], v[96:97], s[6:7] op_sel_hi:[1,0]
	v_exp_f32_e32 v8, v8
	v_exp_f32_e32 v9, v9
	v_exp_f32_e32 v10, v10
	v_exp_f32_e32 v11, v11
	v_pk_mul_f32 v[12:13], v[96:97], v[92:93]
	v_pk_fma_f32 v[8:9], v[8:9], s[18:19], s[18:19] op_sel_hi:[1,0,0]
	v_pk_mul_f32 v[14:15], v[94:95], v[90:91]
	v_pk_fma_f32 v[10:11], v[10:11], s[18:19], s[18:19] op_sel_hi:[1,0,0]
	v_rcp_f32_e32 v8, v8
	v_rcp_f32_e32 v9, v9
	v_rcp_f32_e32 v10, v10
	v_rcp_f32_e32 v11, v11
	v_pk_mul_f32 v[16:17], v[88:89], v[84:85]
	v_pk_mul_f32 v[8:9], v[14:15], v[8:9]
	v_pk_mul_f32 v[14:15], v[88:89], s[6:7] op_sel_hi:[1,0]
	v_pk_mul_f32 v[10:11], v[12:13], v[10:11]
	v_pk_mul_f32 v[12:13], v[86:87], s[6:7] op_sel_hi:[1,0]
	v_exp_f32_e32 v14, v14
	v_exp_f32_e32 v12, v12
	v_exp_f32_e32 v13, v13
	v_exp_f32_e32 v15, v15
	v_pk_mul_f32 v[18:19], v[86:87], v[82:83]
	v_med3_f32 v9, v9, s62, v191
	v_pk_fma_f32 v[12:13], v[12:13], s[18:19], s[18:19] op_sel_hi:[1,0,0]
	v_pk_fma_f32 v[14:15], v[14:15], s[18:19], s[18:19] op_sel_hi:[1,0,0]
	v_rcp_f32_e32 v12, v12
	v_rcp_f32_e32 v13, v13
	v_rcp_f32_e32 v14, v14
	v_rcp_f32_e32 v15, v15
	v_med3_f32 v10, v10, s62, v191
	v_pk_mul_f32 v[12:13], v[18:19], v[12:13]
	v_med3_f32 v11, v11, s62, v191
	v_pk_mul_f32 v[14:15], v[16:17], v[14:15]
	v_med3_f32 v16, v8, s62, v191
	v_mov_b32_e32 v8, 0
	v_cvt_pk_fp8_f32 v8, v16, v9
	v_med3_f32 v12, v12, s62, v191
	v_med3_f32 v13, v13, s62, v191
	v_mov_b32_e32 v9, 0
	v_cvt_pk_fp8_f32 v9, v12, v13
	v_cvt_pk_fp8_f32 v8, v10, v11 op_sel:[0,0,1]
	v_med3_f32 v10, v14, s62, v191
	v_med3_f32 v11, v15, s62, v191
	v_cvt_pk_fp8_f32 v9, v10, v11 op_sel:[0,0,1]
	v_add_u32_e32 v7, 0x80, v6
	v_mad_i64_i32 v[10:11], s[34:35], v7, s63, v[4:5]
	v_lshl_add_u64 v[10:11], v[10:11], 0, v[2:3]
	global_store_dwordx2 v[10:11], v[8:9], off
	v_pk_mul_f32 v[10:11], v[80:81], s[6:7] op_sel_hi:[1,0]
	v_pk_mul_f32 v[8:9], v[78:79], s[6:7] op_sel_hi:[1,0]
	v_exp_f32_e32 v10, v10
	v_exp_f32_e32 v11, v11
	v_exp_f32_e32 v8, v8
	v_exp_f32_e32 v9, v9
	v_pk_mul_f32 v[12:13], v[80:81], v[76:77]
	v_pk_fma_f32 v[10:11], v[10:11], s[18:19], s[18:19] op_sel_hi:[1,0,0]
	v_pk_mul_f32 v[14:15], v[78:79], v[74:75]
	v_rcp_f32_e32 v10, v10
	v_rcp_f32_e32 v11, v11
	v_pk_fma_f32 v[8:9], v[8:9], s[18:19], s[18:19] op_sel_hi:[1,0,0]
	v_pk_mul_f32 v[18:19], v[70:71], v[66:67]
	v_rcp_f32_e32 v8, v8
	v_rcp_f32_e32 v9, v9
	v_pk_mul_f32 v[10:11], v[12:13], v[10:11]
	v_pk_mul_f32 v[12:13], v[70:71], s[6:7] op_sel_hi:[1,0]
	v_pk_mul_f32 v[16:17], v[72:73], v[68:69]
	v_exp_f32_e32 v12, v12
	v_exp_f32_e32 v13, v13
	v_pk_mul_f32 v[8:9], v[14:15], v[8:9]
	v_pk_mul_f32 v[14:15], v[72:73], s[6:7] op_sel_hi:[1,0]
	v_med3_f32 v7, v8, s62, v191
	v_exp_f32_e32 v14, v14
	v_exp_f32_e32 v15, v15
	v_pk_fma_f32 v[12:13], v[12:13], s[18:19], s[18:19] op_sel_hi:[1,0,0]
	v_med3_f32 v9, v9, s62, v191
	v_rcp_f32_e32 v12, v12
	v_rcp_f32_e32 v13, v13
	v_pk_fma_f32 v[14:15], v[14:15], s[18:19], s[18:19] op_sel_hi:[1,0,0]
	v_mov_b32_e32 v8, 0
	v_rcp_f32_e32 v14, v14
	v_rcp_f32_e32 v15, v15
	v_pk_mul_f32 v[12:13], v[18:19], v[12:13]
	v_cvt_pk_fp8_f32 v8, v7, v9
	v_med3_f32 v7, v12, s62, v191
	v_med3_f32 v12, v13, s62, v191
	v_mov_b32_e32 v9, 0
	v_cvt_pk_fp8_f32 v9, v7, v12
	v_pk_mul_f32 v[14:15], v[16:17], v[14:15]
	v_med3_f32 v10, v10, s62, v191
	v_med3_f32 v11, v11, s62, v191
	v_cvt_pk_fp8_f32 v8, v10, v11 op_sel:[0,0,1]
	v_med3_f32 v7, v14, s62, v191
	v_med3_f32 v10, v15, s62, v191
	v_cvt_pk_fp8_f32 v9, v7, v10 op_sel:[0,0,1]
	v_add_u32_e32 v7, 0x90, v6
	v_mad_i64_i32 v[10:11], s[34:35], v7, s63, v[4:5]
	v_lshl_add_u64 v[10:11], v[10:11], 0, v[2:3]
	global_store_dwordx2 v[10:11], v[8:9], off
	v_pk_mul_f32 v[10:11], v[64:65], s[6:7] op_sel_hi:[1,0]
	v_pk_mul_f32 v[8:9], v[62:63], s[6:7] op_sel_hi:[1,0]
	v_exp_f32_e32 v10, v10
	v_exp_f32_e32 v11, v11
	v_exp_f32_e32 v8, v8
	v_exp_f32_e32 v9, v9
	v_pk_mul_f32 v[12:13], v[64:65], v[60:61]
	v_pk_fma_f32 v[10:11], v[10:11], s[18:19], s[18:19] op_sel_hi:[1,0,0]
	v_pk_mul_f32 v[14:15], v[62:63], v[58:59]
	v_rcp_f32_e32 v10, v10
	v_rcp_f32_e32 v11, v11
	v_pk_fma_f32 v[8:9], v[8:9], s[18:19], s[18:19] op_sel_hi:[1,0,0]
	v_pk_mul_f32 v[18:19], v[54:55], v[50:51]
	v_rcp_f32_e32 v8, v8
	v_rcp_f32_e32 v9, v9
	v_pk_mul_f32 v[10:11], v[12:13], v[10:11]
	v_pk_mul_f32 v[12:13], v[54:55], s[6:7] op_sel_hi:[1,0]
	v_pk_mul_f32 v[16:17], v[56:57], v[52:53]
	v_exp_f32_e32 v12, v12
	v_exp_f32_e32 v13, v13
	v_pk_mul_f32 v[8:9], v[14:15], v[8:9]
	v_pk_mul_f32 v[14:15], v[56:57], s[6:7] op_sel_hi:[1,0]
	v_med3_f32 v7, v8, s62, v191
	v_exp_f32_e32 v14, v14
	v_exp_f32_e32 v15, v15
	v_pk_fma_f32 v[12:13], v[12:13], s[18:19], s[18:19] op_sel_hi:[1,0,0]
	v_med3_f32 v9, v9, s62, v191
	v_rcp_f32_e32 v12, v12
	v_rcp_f32_e32 v13, v13
	v_pk_fma_f32 v[14:15], v[14:15], s[18:19], s[18:19] op_sel_hi:[1,0,0]
	v_mov_b32_e32 v8, 0
	v_rcp_f32_e32 v14, v14
	v_rcp_f32_e32 v15, v15
	v_pk_mul_f32 v[12:13], v[18:19], v[12:13]
	v_cvt_pk_fp8_f32 v8, v7, v9
	v_med3_f32 v7, v12, s62, v191
	v_med3_f32 v12, v13, s62, v191
	v_mov_b32_e32 v9, 0
	v_cvt_pk_fp8_f32 v9, v7, v12
	v_pk_mul_f32 v[14:15], v[16:17], v[14:15]
	v_med3_f32 v10, v10, s62, v191
	v_med3_f32 v11, v11, s62, v191
	v_cvt_pk_fp8_f32 v8, v10, v11 op_sel:[0,0,1]
	v_med3_f32 v7, v14, s62, v191
	v_med3_f32 v10, v15, s62, v191
	v_cvt_pk_fp8_f32 v9, v7, v10 op_sel:[0,0,1]
	v_add_u32_e32 v7, 0xa0, v6
	v_mad_i64_i32 v[10:11], s[34:35], v7, s63, v[4:5]
	v_lshl_add_u64 v[10:11], v[10:11], 0, v[2:3]
	global_store_dwordx2 v[10:11], v[8:9], off
	v_pk_mul_f32 v[10:11], v[48:49], s[6:7] op_sel_hi:[1,0]
	v_pk_mul_f32 v[8:9], v[46:47], s[6:7] op_sel_hi:[1,0]
	v_exp_f32_e32 v10, v10
	v_exp_f32_e32 v11, v11
	v_exp_f32_e32 v8, v8
	v_exp_f32_e32 v9, v9
	v_pk_mul_f32 v[12:13], v[48:49], v[44:45]
	v_pk_fma_f32 v[10:11], v[10:11], s[18:19], s[18:19] op_sel_hi:[1,0,0]
	v_pk_mul_f32 v[14:15], v[46:47], v[42:43]
	v_rcp_f32_e32 v10, v10
	v_rcp_f32_e32 v11, v11
	v_pk_fma_f32 v[8:9], v[8:9], s[18:19], s[18:19] op_sel_hi:[1,0,0]
	v_pk_mul_f32 v[18:19], v[38:39], v[34:35]
	v_rcp_f32_e32 v8, v8
	v_rcp_f32_e32 v9, v9
	v_pk_mul_f32 v[10:11], v[12:13], v[10:11]
	v_pk_mul_f32 v[12:13], v[38:39], s[6:7] op_sel_hi:[1,0]
	v_pk_mul_f32 v[16:17], v[40:41], v[36:37]
	v_exp_f32_e32 v12, v12
	v_exp_f32_e32 v13, v13
	v_pk_mul_f32 v[8:9], v[14:15], v[8:9]
	v_pk_mul_f32 v[14:15], v[40:41], s[6:7] op_sel_hi:[1,0]
	v_med3_f32 v7, v8, s62, v191
	v_exp_f32_e32 v14, v14
	v_exp_f32_e32 v15, v15
	v_pk_fma_f32 v[12:13], v[12:13], s[18:19], s[18:19] op_sel_hi:[1,0,0]
	v_med3_f32 v9, v9, s62, v191
	v_rcp_f32_e32 v12, v12
	v_rcp_f32_e32 v13, v13
	v_pk_fma_f32 v[14:15], v[14:15], s[18:19], s[18:19] op_sel_hi:[1,0,0]
	v_mov_b32_e32 v8, 0
	v_rcp_f32_e32 v14, v14
	v_rcp_f32_e32 v15, v15
	v_pk_mul_f32 v[12:13], v[18:19], v[12:13]
	v_cvt_pk_fp8_f32 v8, v7, v9
	v_med3_f32 v7, v12, s62, v191
	v_med3_f32 v12, v13, s62, v191
	v_mov_b32_e32 v9, 0
	v_cvt_pk_fp8_f32 v9, v7, v12
	v_pk_mul_f32 v[14:15], v[16:17], v[14:15]
	v_med3_f32 v10, v10, s62, v191
	v_med3_f32 v11, v11, s62, v191
	v_cvt_pk_fp8_f32 v8, v10, v11 op_sel:[0,0,1]
	v_med3_f32 v7, v14, s62, v191
	v_med3_f32 v10, v15, s62, v191
	v_cvt_pk_fp8_f32 v9, v7, v10 op_sel:[0,0,1]
	v_add_u32_e32 v6, 0xb0, v6
	v_mad_i64_i32 v[4:5], s[34:35], v6, s63, v[4:5]
	v_lshl_add_u64 v[2:3], v[4:5], 0, v[2:3]
	s_andn2_b64 vcc, exec, s[4:5]
	s_mov_b64 s[4:5], -1
	s_mov_b32 s66, s74
	global_store_dwordx2 v[2:3], v[8:9], off
	s_cbranch_vccnz .LBB0_2362
	s_andn2_b64 vcc, exec, s[8:9]
	s_cbranch_vccnz .LBB0_2361
	s_mov_b32 s101, 1
	s_branch .LBB0_2361

.LBB0_2427:
	s_mov_b32 s101, 0
	s_mov_b32 s100, 0
	s_cmp_lt_i32 s78, 20
	s_cselect_b64 s[2:3], -1, 0
	s_and_b64 s[2:3], s[2:3], s[4:5]
	s_and_b64 s[0:1], s[2:3], s[0:1]
	s_andn2_b64 vcc, exec, s[0:1]
	s_cbranch_vccnz .LBB0_2448
	s_lshl_b32 s6, s58, 3
	v_readlane_b32 s0, v254, 14
	s_cmp_ge_i32 s0, s6
	v_readfirstlane_b32 s4, v0
	s_cbranch_scc1 .LBB0_2448
	v_lshrrev_b32_e32 v1, 5, v0
	v_and_b32_e32 v2, 4, v1
	v_lshrrev_b32_e32 v1, 1, v0
	v_bfe_u32 v3, v0, 2, 2
	v_and_b32_e32 v1, 24, v1
	v_bfe_u32 v4, v0, 3, 25
	s_add_u32 s42, s86, 0x2dc00000
	v_or3_b32 v2, v2, v3, v1
	v_lshlrev_b32_e32 v3, 4, v0
	v_or_b32_e32 v4, 64, v4
	s_movk_i32 s0, 0x60
	s_waitcnt lgkmcnt(0)
	v_and_b32_e32 v6, 32, v0
	s_addc_u32 s43, s87, 0
	v_and_or_b32 v5, v4, s0, v2
	v_bitop3_b32 v10, v3, v6, 48 bitop3:0x6c
	v_and_b32_e32 v11, 64, v0
	s_add_u32 s8, s86, 0x16800000
	v_mul_u32_u24_e32 v5, 0x1c00, v5
	v_or_b32_e32 v3, v10, v11
	v_readlane_b32 s7, v254, 14
	s_addc_u32 s9, s87, 0
	s_waitcnt vmcnt(0)
	v_or_b32_e32 v160, v5, v3
	v_bfe_u32 v5, v0, 2, 4
	s_movk_i32 s0, 0x70
	s_ashr_i32 s45, s7, 31
	v_and_or_b32 v4, v4, s0, v5
	s_lshr_b32 s0, s45, 29
	s_add_i32 s0, s7, s0
	s_lshr_b32 s18, s4, 6
	s_ashr_i32 s1, s0, 3
	s_and_b32 s0, s0, -8
	s_lshr_b32 s5, s4, 8
	s_lshl_b32 s44, s18, 10
	s_sub_i32 s0, s7, s0
	s_add_i32 s46, s58, 1
	s_cmp_lt_i32 s0, 0
	s_cselect_b32 s7, s46, s58
	s_mul_i32 s0, s7, s0
	s_add_i32 s0, s0, s1
	s_ashr_i32 s1, s0, 31
	s_lshr_b32 s1, s1, 26
	s_add_i32 s1, s0, s1
	s_ashr_i32 s7, s1, 6
	s_lshl_b32 s7, s7, 3
	v_mul_u32_u24_e32 v12, 0x1c00, v4
	v_lshrrev_b32_e32 v4, 3, v0
	s_sub_i32 s10, s58, s7
	v_and_or_b32 v2, v4, 32, v2
	s_min_i32 s10, s10, 8
	v_mul_u32_u24_e32 v2, 0x1c00, v2
	s_abs_i32 s11, s10
	v_or_b32_e32 v164, v2, v3
	v_cvt_f32_u32_e32 v2, s11
	s_sub_i32 s13, 0, s11
	s_andn2_b32 s1, s1, 63
	s_sub_i32 s0, s0, s1
	v_rcp_iflag_f32_e32 v2, v2
	s_abs_i32 s12, s0
	s_xor_b32 s1, s0, s10
	s_ashr_i32 s1, s1, 31
	v_mul_f32_e32 v2, 0x4f7ffffe, v2
	v_cvt_u32_f32_e32 v2, v2
	v_and_or_b32 v4, v4, 48, v5
	v_mul_u32_u24_e32 v13, 0x1c00, v4
	v_or_b32_e32 v162, v12, v3
	v_readfirstlane_b32 s16, v2
	s_mul_i32 s13, s13, s16
	s_mul_hi_u32 s13, s16, s13
	s_add_i32 s16, s16, s13
	s_mul_hi_u32 s13, s12, s16
	s_mul_i32 s16, s13, s11
	s_sub_i32 s12, s12, s16
	s_add_i32 s16, s13, 1
	s_sub_i32 s17, s12, s11
	s_cmp_ge_u32 s12, s11
	s_cselect_b32 s13, s16, s13
	s_cselect_b32 s12, s17, s12
	s_add_i32 s16, s13, 1
	s_cmp_ge_u32 s12, s11
	s_cselect_b32 s11, s16, s13
	s_xor_b32 s11, s11, s1
	s_sub_i32 s69, s11, s1
	s_mul_i32 s1, s69, s10
	s_sub_i32 s0, s0, s1
	s_add_i32 s70, s7, s0
	s_cmp_ge_i32 s70, s33
	s_cselect_b64 s[0:1], -1, 0
	s_cmp_ge_i32 s70, s57
	v_cndmask_b32_e64 v2, 0, 1, s[0:1]
	s_cselect_b64 s[0:1], -1, 0
	s_cmp_ge_i32 s70, s52
	v_or_b32_e32 v166, v13, v3
	v_cndmask_b32_e64 v3, 0, 1, s[0:1]
	s_cselect_b64 s[0:1], -1, 0
	v_readfirstlane_b32 s7, v2
	v_readfirstlane_b32 s10, v3
	s_cmp_lg_u64 s[0:1], 0
	s_addc_u32 s7, s7, s10
	s_cmp_ge_i32 s70, s53
	s_cselect_b64 s[0:1], -1, 0
	s_cmp_ge_i32 s70, s54
	v_cndmask_b32_e64 v2, 0, 1, s[0:1]
	s_cselect_b64 s[0:1], -1, 0
	v_readfirstlane_b32 s10, v2
	s_cmp_lg_u64 s[0:1], 0
	s_addc_u32 s7, s7, s10
	s_cmp_ge_i32 s70, s55
	s_cselect_b64 s[0:1], -1, 0
	s_cmp_ge_i32 s70, s56
	v_cndmask_b32_e64 v2, 0, 1, s[0:1]
	s_cselect_b64 s[0:1], -1, 0
	v_readfirstlane_b32 s10, v2
	s_cmp_lg_u64 s[0:1], 0
	s_addc_u32 s0, s7, s10
	s_lshl_b32 s0, s0, 3
	s_add_i32 s0, s0, s69
	s_mul_hi_i32 s1, s0, 0x1c0000
	s_mul_i32 s0, s0, 0x1c0000
	s_add_u32 s0, s8, s0
	s_addc_u32 s1, s9, s1
	s_add_i32 s47, s44, 0
	s_add_i32 m0, s47, 0x10000
	s_mul_i32 s12, s70, 0x1c0000
	global_load_lds_dwordx4 v164, s[0:1]
	s_add_i32 m0, s47, 0x12000
	s_add_u32 s10, s0, 0xe0000
	global_load_lds_dwordx4 v160, s[0:1]
	s_addc_u32 s11, s1, 0
	s_add_i32 m0, s47, 0x14000
	s_mul_hi_i32 s7, s70, 0x1c0000
	global_load_lds_dwordx4 v164, s[10:11]
	s_add_i32 m0, s47, 0x16000
	s_add_u32 s38, s42, s12
	s_addc_u32 s39, s43, s7
	s_add_i32 s48, s47, 0x2000
	global_load_lds_dwordx4 v160, s[10:11]
	s_mov_b32 m0, s47
	s_add_u32 s10, s38, 0xe0000
	global_load_lds_dwordx4 v166, s[38:39]
	s_mov_b32 m0, s48
	s_addc_u32 s11, s39, 0
	s_add_i32 s49, s47, 0x4000
	global_load_lds_dwordx4 v162, s[38:39]
	s_mov_b32 m0, s49
	s_add_i32 s50, s47, 0x6000
	global_load_lds_dwordx4 v166, s[10:11]
	s_mov_b32 m0, s50
	v_mov_b32_e32 v165, 0
	global_load_lds_dwordx4 v162, s[10:11]
	v_mov_b32_e32 v161, v165
	v_mov_b32_e32 v167, v165
	v_mov_b32_e32 v163, v165
	s_cmp_eq_u32 s5, 1
	s_mov_b32 s7, 0
	s_mov_b32 s51, 0x1c0000
	v_lshl_add_u64 v[8:9], s[0:1], 0, v[164:165]
	v_lshl_add_u64 v[4:5], s[0:1], 0, v[160:161]
	s_mov_b64 s[10:11], 0xe0000
	v_lshl_add_u64 v[2:3], s[38:39], 0, v[166:167]
	s_cselect_b64 s[12:13], -1, 0
	s_cmp_lg_u32 s5, 1
	v_lshl_add_u64 v[6:7], s[38:39], 0, v[162:163]
	s_cbranch_scc1 .LBB0_2431
	s_barrier

.LBB0_2440:
	s_add_u32 s38, s38, 0xe0080
	s_addc_u32 s39, s39, 0
	v_lshl_add_u64 v[176:177], v[0:1], 0, s[26:27]
	s_mov_b32 s71, -2
	s_cmp_lg_u32 s101, 0
	s_cbranch_scc0 .Lbs_2441
	s_barrier
	s_mov_b32 s101, 0
.Lbs_2441:
	ds_read_b128 v[16:19], v191
	ds_read_b128 v[20:23], v191 offset:1024
	ds_read_b128 v[24:27], v191 offset:2048
	ds_read_b128 v[28:31], v191 offset:3072
	ds_read_b128 v[0:3], v192
	ds_read_b128 v[4:7], v192 offset:1024
	ds_read_b128 v[8:11], v192 offset:2048
	ds_read_b128 v[12:15], v192 offset:3072
	s_add_u32 s40, s38, 0xfff20080
	s_addc_u32 s41, s39, -1
	s_cmp_eq_u32 s71, 52
	s_cselect_b64 vcc, -1, 0
	s_cselect_b32 s41, s1, s41
	s_cselect_b32 s40, s0, s40
	v_cndmask_b32_e32 v179, v177, v175, vcc
	v_cndmask_b32_e32 v178, v176, v174, vcc
	v_lshl_add_u64 v[214:215], s[38:39], 0, v[168:169]
	s_add_i32 m0, s47, 0xc000
	ds_read_b128 v[180:183], v193
	ds_read_b128 v[184:187], v193 offset:1024
	ds_read_b128 v[198:201], v193 offset:2048
	ds_read_b128 v[202:205], v193 offset:3072
	ds_read_b128 v[206:209], v193 offset:4096
	ds_read_b128 v[210:213], v193 offset:5120
	ds_read_b128 v[216:219], v193 offset:6144
	ds_read_b128 v[220:223], v193 offset:7168
	global_load_lds_dwordx4 v[214:215], off
	v_lshl_add_u64 v[214:215], s[38:39], 0, v[170:171]
	s_add_i32 m0, s47, 0xe000
	s_nop 0
	global_load_lds_dwordx4 v[214:215], off
	s_cmp_lg_u32 s100, 0
	s_cbranch_scc1 .Lrx_2441_0
	s_waitcnt vmcnt(8)

.LBB0_2444:
	v_lshl_add_u32 v6, s70, 8, v188
	v_lshl_or_b32 v0, s69, 8, v190
	v_ashrrev_i32_e32 v7, 31, v6
	v_ashrrev_i32_e32 v1, 31, v0
	v_lshlrev_b64 v[2:3], 12, v[6:7]
	v_lshl_add_u64 v[2:3], s[16:17], 0, v[2:3]
	v_lshlrev_b64 v[8:9], 1, v[0:1]
	s_nop 15
	s_nop 15
	v_lshl_add_u64 v[0:1], v[2:3], 0, v[8:9]
	v_cvt_pk_bf16_f32 v2, v156, v157
	v_cvt_pk_bf16_f32 v3, v158, v159
	v_cvt_pk_bf16_f32 v4, v152, v153
	v_cvt_pk_bf16_f32 v5, v154, v155
	global_store_dwordx4 v[0:1], v[2:5], off
	s_nop 1
	v_cvt_pk_bf16_f32 v2, v144, v145
	v_cvt_pk_bf16_f32 v3, v146, v147
	v_cvt_pk_bf16_f32 v4, v136, v137
	v_cvt_pk_bf16_f32 v5, v138, v139
	global_store_dwordx4 v[0:1], v[2:5], off offset:256
	s_nop 1
	v_or_b32_e32 v2, 16, v6
	v_ashrrev_i32_e32 v3, 31, v2
	v_lshlrev_b64 v[2:3], 12, v[2:3]
	v_lshl_add_u64 v[2:3], s[16:17], 0, v[2:3]
	v_lshl_add_u64 v[10:11], v[2:3], 0, v[8:9]
	v_cvt_pk_bf16_f32 v2, v148, v149
	v_cvt_pk_bf16_f32 v3, v150, v151
	v_cvt_pk_bf16_f32 v4, v140, v141
	v_cvt_pk_bf16_f32 v5, v142, v143
	global_store_dwordx4 v[10:11], v[2:5], off
	s_nop 1
	v_cvt_pk_bf16_f32 v2, v128, v129
	v_cvt_pk_bf16_f32 v3, v130, v131
	v_cvt_pk_bf16_f32 v4, v120, v121
	v_cvt_pk_bf16_f32 v5, v122, v123
	global_store_dwordx4 v[10:11], v[2:5], off offset:256
	s_nop 1
	v_or_b32_e32 v2, 32, v6
	v_ashrrev_i32_e32 v3, 31, v2
	v_lshlrev_b64 v[2:3], 12, v[2:3]
	v_lshl_add_u64 v[2:3], s[16:17], 0, v[2:3]
	v_lshl_add_u64 v[10:11], v[2:3], 0, v[8:9]
	v_cvt_pk_bf16_f32 v2, v132, v133
	v_cvt_pk_bf16_f32 v3, v134, v135
	v_cvt_pk_bf16_f32 v4, v124, v125
	v_cvt_pk_bf16_f32 v5, v126, v127
	global_store_dwordx4 v[10:11], v[2:5], off
	s_nop 1
	v_cvt_pk_bf16_f32 v2, v112, v113
	v_cvt_pk_bf16_f32 v3, v114, v115
	v_cvt_pk_bf16_f32 v4, v104, v105
	v_cvt_pk_bf16_f32 v5, v106, v107
	global_store_dwordx4 v[10:11], v[2:5], off offset:256
	s_nop 1
	v_or_b32_e32 v2, 48, v6
	v_ashrrev_i32_e32 v3, 31, v2
	v_lshlrev_b64 v[2:3], 12, v[2:3]
	v_lshl_add_u64 v[2:3], s[16:17], 0, v[2:3]
	v_lshl_add_u64 v[6:7], v[2:3], 0, v[8:9]
	v_cvt_pk_bf16_f32 v2, v116, v117
	v_cvt_pk_bf16_f32 v3, v118, v119
	v_cvt_pk_bf16_f32 v4, v108, v109
	v_cvt_pk_bf16_f32 v5, v110, v111
	global_store_dwordx4 v[6:7], v[2:5], off
	v_add_co_u32_e32 v8, vcc, s63, v0
	s_nop 0
	v_cvt_pk_bf16_f32 v2, v100, v101
	v_cvt_pk_bf16_f32 v3, v102, v103
	v_cvt_pk_bf16_f32 v4, v96, v97
	v_cvt_pk_bf16_f32 v5, v98, v99
	global_store_dwordx4 v[6:7], v[2:5], off offset:256
	v_addc_co_u32_e32 v9, vcc, 0, v1, vcc
	s_nop 0
	v_cvt_pk_bf16_f32 v2, v92, v93
	v_cvt_pk_bf16_f32 v3, v94, v95
	v_cvt_pk_bf16_f32 v4, v88, v89
	v_cvt_pk_bf16_f32 v5, v90, v91
	v_lshl_add_u64 v[6:7], v[0:1], 0, s[28:29]
	global_store_dwordx4 v[8:9], v[2:5], off
	v_add_co_u32_e32 v8, vcc, s64, v0
	s_nop 0
	v_cvt_pk_bf16_f32 v2, v80, v81
	v_cvt_pk_bf16_f32 v3, v82, v83
	v_cvt_pk_bf16_f32 v4, v72, v73
	v_cvt_pk_bf16_f32 v5, v74, v75
	global_store_dwordx4 v[6:7], v[2:5], off offset:256
	v_addc_co_u32_e32 v9, vcc, 0, v1, vcc
	s_nop 0
	v_cvt_pk_bf16_f32 v2, v84, v85
	v_cvt_pk_bf16_f32 v3, v86, v87
	v_cvt_pk_bf16_f32 v4, v76, v77
	v_cvt_pk_bf16_f32 v5, v78, v79
	v_lshl_add_u64 v[6:7], v[0:1], 0, s[30:31]
	global_store_dwordx4 v[8:9], v[2:5], off
	v_add_co_u32_e32 v8, vcc, s65, v0
	s_nop 0
	v_cvt_pk_bf16_f32 v2, v64, v65
	v_cvt_pk_bf16_f32 v3, v66, v67
	v_cvt_pk_bf16_f32 v4, v56, v57
	v_cvt_pk_bf16_f32 v5, v58, v59
	global_store_dwordx4 v[6:7], v[2:5], off offset:256
	v_lshl_add_u64 v[6:7], v[0:1], 0, s[34:35]
	v_addc_co_u32_e32 v9, vcc, 0, v1, vcc
	v_cvt_pk_bf16_f32 v2, v68, v69
	v_cvt_pk_bf16_f32 v3, v70, v71
	v_cvt_pk_bf16_f32 v4, v60, v61
	v_cvt_pk_bf16_f32 v5, v62, v63
	global_store_dwordx4 v[8:9], v[2:5], off
	s_nop 1
	v_cvt_pk_bf16_f32 v2, v48, v49
	v_cvt_pk_bf16_f32 v3, v50, v51
	v_cvt_pk_bf16_f32 v4, v40, v41
	v_cvt_pk_bf16_f32 v5, v42, v43
	global_store_dwordx4 v[6:7], v[2:5], off offset:256
	v_lshl_add_u64 v[6:7], v[0:1], 0, s[36:37]
	v_add_co_u32_e32 v0, vcc, s66, v0
	v_cvt_pk_bf16_f32 v2, v52, v53
	v_cvt_pk_bf16_f32 v3, v54, v55
	v_cvt_pk_bf16_f32 v4, v44, v45
	v_cvt_pk_bf16_f32 v5, v46, v47
	s_nop 1
	v_addc_co_u32_e32 v1, vcc, 0, v1, vcc
	s_and_b64 vcc, exec, s[4:5]
	s_mov_b64 s[4:5], -1
	global_store_dwordx4 v[0:1], v[2:5], off
	v_cvt_pk_bf16_f32 v0, v36, v37
	v_cvt_pk_bf16_f32 v1, v38, v39
	s_nop 1
	v_cvt_pk_bf16_f32 v2, v32, v33
	v_cvt_pk_bf16_f32 v3, v34, v35
	global_store_dwordx4 v[6:7], v[0:3], off offset:256
	s_cbranch_vccnz .LBB0_2433
	s_andn2_b64 vcc, exec, s[12:13]
	s_cbranch_vccnz .LBB0_2432
	s_mov_b32 s101, 1
	s_branch .LBB0_2432
